# ILC6: expert-weight f32->fp8 conversion hosted in both attention tile loops (16 slots in phase-4 diff loop, 33 in MLA loop), credit-scheduled, wave-group staggered, counted vmcnt waits; queue disabled
# speedup vs baseline: 1.0180x; 1.0087x over previous
; #define VM_WAIT() asm volatile("s_waitcnt vmcnt(0)" ::: "memory")
;     ...
;             const bf16* Qw = P.U + (size_t)qrow * UW + U_DF + h * 128 + pass * 64 + hi * 8;
; #pragma unroll
;             for (int d0 = 0; d0 < 4; ++d0) qr[d0] = *(const bf16x8*)(Qw + d0 * 16);
;     ...
;         unsigned gsv[2], gsk[2], gsk2 = 0u;
; #pragma unroll
;         for (int i = 0; i < 2; ++i) { const int a = (i * 512 + tid) * 16;
;             { const int sub = a >> 9, within = a & 511; const int kk = (sub >> 2) * 8 + (within >> 6); const int k = (kk & ~0xC) | ((kk & 4) << 1) | ((kk & 8) >> 1);
;               const int c = (sub & 3) * 32 + ((within & 63) >> 1); gsv[i] = (unsigned)(k * ldv + c) * 2u; }
;             if constexpr (MODE == MODE_DIFF) { if (i == 0) { const int row = a >> 7, ch = ((a >> 4) & 7) ^ ((row >> 1) & 7); gsk[0] = (unsigned)(row * ldk + ch * 8) * 2u; } gsk[1] = 0u; }
;             else { const int row = a >> 8, ch = ((a >> 4) & 15) ^ (row & 15); gsk[i] = (unsigned)(row * ldk + ch * 8) * 2u; } }
;         if constexpr (MODE == MODE_MLA) { const int a = tid * 16, row = a >> 7, ch = ((a >> 4) & 7) ^ ((row >> 1) & 7); gsk2 = (unsigned)(row * UW + ch * 8) * 2u; }
;         const unsigned ldsw = (unsigned)__builtin_amdgcn_readfirstlane(wid) * 1024u;
;     ...
;         f32x16 pB0, pB1; float mnB, alB;
;         GLDS3(0); GLDS3(1); VM_WAIT(); __syncthreads();
.LBB0_485:
	s_getreg_b32 s1, hwreg(HW_REG_HW_ID, 0, 6)
	s_and_b32 s1, s1, 63
	s_lshl_b32 s1, s1, 2
	s_add_i32 s1, s1, 0
	s_add_i32 s1, s1, 0x23f00
	v_mov_b32_e32 v0, s1
	ds_read_b32 v140, v0
	s_waitcnt lgkmcnt(0)
	v_readfirstlane_b32 s39, v140
	s_lshr_b32 s52, s39, 2
	s_mul_i32 s52, s52, 15
	v_readlane_b32 s46, v254, 43
	s_and_b32 s47, s46, 63
	s_lshl_b32 s47, s47, 3
	s_add_u32 s39, s47, s39
	s_lshr_b32 s54, s46, 6
	v_mbcnt_lo_u32_b32 v223, -1, 0
	v_mbcnt_hi_u32_b32 v223, -1, v223
	v_lshrrev_b32_e32 v226, 3, v223
	v_and_b32_e32 v229, 7, v223
	v_readlane_b32 s56, v254, 62
	s_lshr_b32 s56, s56, 3
	v_readlane_b32 s36, v254, 44
	v_readlane_b32 s37, v254, 45
	v_readlane_b32 s34, v254, 46
	v_readlane_b32 s35, v254, 47
	s_sub_u32 s34, s34, 0x4000
	s_subb_u32 s35, s35, 0
	s_mov_b32 s42, 0
	s_mov_b32 s51, 0
	s_mov_b32 s53, 0
	s_lshl_b32 s0, s2, 19
	s_and_b32 s9, s0, 0x2000000
	s_lshl_b32 s0, s96, 4
	s_and_b32 s8, s0, 0x70
	s_lshl_b32 s10, s96, 5
	v_writelane_b32 v255, s2, 26
	s_cmpk_lt_u32 s96, 0x80
	s_mov_b64 s[0:1], -1
	s_cbranch_scc1 .LBB0_497
	v_readlane_b32 s0, v255, 26
	s_lshl_b32 s0, s0, 4
	s_and_b32 s0, s0, 0x300
	s_add_u32 s0, s9, s0
	s_addc_u32 s1, 0, 0
	v_readlane_b32 s2, v255, 6
	v_readlane_b32 s3, v255, 7
	s_add_u32 s6, s2, s0
	s_waitcnt lgkmcnt(0)
	v_readfirstlane_b32 s0, v140
	s_addc_u32 s7, s3, s1
	v_mbcnt_lo_u32_b32 v0, -1, 0
	v_mbcnt_hi_u32_b32 v0, -1, v0
	v_mov_b32_e32 v113, v193
	v_lshl_add_u32 v4, s0, 6, v0
	s_lshl_b32 s0, s8, 6
	s_and_b32 s2, s0, 0x1000
	s_and_b32 s0, s10, 0xf00
	s_or_b32 s11, s2, s0
	v_ashrrev_i32_e32 v143, 6, v4
	v_and_b32_e32 v72, 63, v4
	v_and_b32_e32 v1, 0x3fffffc0, v4
	s_add_i32 s0, 0, 0x1e000
	v_lshlrev_b32_e32 v5, 4, v4
	v_and_b32_e32 v141, 31, v4
	v_lshl_add_u32 v0, v143, 5, s11
	v_lshl_add_u32 v144, v1, 2, s0
	v_lshlrev_b32_e32 v1, 3, v72
	v_and_b32_e32 v2, 0xc0, v5
	v_lshlrev_b32_e32 v6, 1, v4
	v_or_b32_e32 v0, v0, v141
	v_and_or_b32 v2, v1, 24, v2
	v_and_b32_e32 v3, 32, v6
	v_and_b32_e32 v1, 0x100, v1
	v_or3_b32 v147, v2, v3, v1
	s_lshl_b32 s0, s8, 3
	v_ashrrev_i32_e32 v1, 31, v0
	s_and_b32 s12, s0, 0x180
	v_lshlrev_b64 v[0:1], 13, v[0:1]
	v_bfe_u32 v142, v4, 5, 1
	v_lshl_add_u64 v[0:1], s[84:85], 0, v[0:1]
	s_lshl_b32 s68, s12, 1
	v_lshl_add_u64 v[0:1], v[0:1], 0, s[68:69]
	v_lshlrev_b32_e32 v112, 4, v142
	v_lshl_add_u64 v[0:1], v[0:1], 0, v[112:113]
	s_mov_b64 s[0:1], 0x1480
	v_lshl_add_u64 v[2:3], v[0:1], 0, s[0:1]
	s_movk_i32 s0, 0x1000
	v_add_co_u32_e32 v0, vcc, s0, v0
	v_readlane_b32 s0, v255, 15
	s_nop 0
	v_addc_co_u32_e32 v1, vcc, 0, v1, vcc
	global_load_dwordx4 v[104:107], v[0:1], off offset:1152
	global_load_dwordx4 v[108:111], v[2:3], off offset:32
	global_load_dwordx4 v[100:103], v[2:3], off offset:64
	global_load_dwordx4 v[96:99], v[2:3], off offset:96
	v_lshrrev_b32_e32 v2, 4, v4
	s_add_u32 s4, s0, s68
	v_readlane_b32 s0, v255, 16
	v_xor_b32_e32 v2, v2, v4
	v_lshlrev_b32_e32 v3, 10, v4
	s_addc_u32 s5, s0, 0
	v_and_b32_e32 v3, 0xffffe000, v3
	v_lshlrev_b32_e32 v2, 4, v2
	s_movk_i32 s19, 0x70
	v_and_or_b32 v192, v2, s19, v3
	v_bfe_i32 v2, v4, 4, 24
	s_add_u32 s0, s84, s68
	v_bfe_u32 v0, v4, 2, 2
	v_lshrrev_b32_e32 v1, 1, v4
	v_and_b32_e32 v3, 0x7fff0, v2
	v_lshrrev_b32_e32 v2, 1, v2
	s_addc_u32 s1, s85, 0
	v_and_or_b32 v0, v1, 8, v0
	v_and_b32_e32 v2, 4, v2
	s_add_u32 s15, s0, 0x1880
	v_readfirstlane_b32 s0, v143
	v_or3_b32 v2, v3, v2, v0
	v_add_u32_e32 v3, 0x2000, v5
	s_addc_u32 s16, s1, 0
	s_lshl_b32 s13, s0, 10
	s_lshl_b32 s17, s2, 13
	v_ashrrev_i32_e32 v3, 8, v3
	s_add_u32 s0, s4, s17
	v_and_b32_e32 v74, 48, v5
	v_and_b32_e32 v5, 0x7fff0, v3
	v_lshrrev_b32_e32 v3, 1, v3
	s_addc_u32 s1, s5, 0
	v_and_b32_e32 v73, 0xc0, v6
	v_and_b32_e32 v3, 4, v3
	s_add_u32 s2, s15, s17
	v_or_b32_e32 v1, v74, v73
	v_lshlrev_b32_e32 v75, 13, v2
	v_or3_b32 v0, v5, v3, v0
	s_addc_u32 s3, s16, 0
	s_add_i32 s14, s13, 0
	v_or_b32_e32 v2, v75, v1
	v_lshlrev_b32_e32 v76, 13, v0
	s_mov_b32 m0, s14
	v_or_b32_e32 v0, v76, v1
	s_add_i32 s18, s14, 0xc000
	global_load_lds_dwordx4 v2, s[0:1]
	s_add_i32 m0, s14, 0x2000
	s_bitset1_b32 s17, 19
	global_load_lds_dwordx4 v0, s[0:1]
	s_add_u32 s0, s4, s17
	s_mov_b32 m0, s18
	s_addc_u32 s1, s5, 0
	global_load_lds_dwordx4 v192, s[2:3]
	s_add_u32 s2, s15, s17
	s_addc_u32 s3, s16, 0
	s_add_i32 m0, s14, 0x4000
	s_add_i32 s4, s14, 0x12000
	global_load_lds_dwordx4 v2, s[0:1]
	s_add_i32 m0, s14, 0x6000
	v_lshlrev_b32_e32 v148, 7, v141
	global_load_lds_dwordx4 v0, s[0:1]
	s_mov_b32 m0, s4
	v_lshlrev_b32_e32 v0, 3, v4
	global_load_lds_dwordx4 v192, s[2:3]
	v_and_b32_e32 v4, 0x70, v0
	v_bitop3_b32 v150, v112, v0, s19 bitop3:0x78
	v_add_u32_e32 v152, 0, v148
	v_bitop3_b32 v154, v112, v4, 32 bitop3:0x36
	v_bitop3_b32 v155, v112, v4, 64 bitop3:0x36
	v_add_u32_e32 v149, v152, v150
	v_add_u32_e32 v151, v152, v154
	v_add_u32_e32 v153, v152, v155
	s_waitcnt vmcnt(0)
	s_waitcnt vmcnt(0) lgkmcnt(0)
	s_barrier
; #define VM_WAIT() asm volatile("s_waitcnt vmcnt(0)" ::: "memory")
; template <int MODE>
; __device__ __forceinline__ void partialSM(f32x16& p0, f32x16& p1, float& m_reg, float& mn, float& alpha) {
;     constexpr float SCALE = Cfg<MODE>::SCALE, C = SCALE * LOG2E;
;     float pmax = p0[0];
; #pragma unroll
;     for (int r = 1; r < 16; ++r) pmax = fmaxf(pmax, p0[r]);
; #pragma unroll
;     for (int r = 0; r < 16; ++r) pmax = fmaxf(pmax, p1[r]);
;     { auto rr = __builtin_amdgcn_permlane32_swap(__float_as_uint(pmax), __float_as_uint(pmax), false, false);
;       pmax = fmaxf(__uint_as_float(rr[0]), __uint_as_float(rr[1])); }
;     if (__builtin_expect(__all(pmax - m_reg <= THR / SCALE), 1)) { mn = m_reg; alpha = 1.f; }
;     else { mn = fmaxf(m_reg, pmax); alpha = __builtin_amdgcn_exp2f((m_reg - mn) * C); m_reg = mn; }
;     const float mnC = -mn * C;
; #pragma unroll
;     for (int r = 0; r < 16; ++r) p0[r] = fmaf(p0[r], C, mnC);
; #pragma unroll
;     for (int r = 0; r < 16; ++r) p1[r] = fmaf(p1[r], C, mnC);
; #pragma unroll
;     for (int r = 0; r < 16; ++r) p0[r] = __builtin_amdgcn_exp2f(p0[r]);
; }
;     ...
;         GLDS3(0); GLDS3(1); VM_WAIT(); __syncthreads();
;         qkt<MODE>(p0, p1, KB3(0), qr, r32, hi); partialSM<MODE>(p0, p1, m_reg, mn, al);
	ds_read_b128 v[0:3], v149 offset:49152
	ds_read_b128 v[16:19], v149 offset:53248
	ds_read_b128 v[48:51], v151 offset:49152
	ds_read_b128 v[52:55], v151 offset:53248
	ds_read_b128 v[56:59], v153 offset:49152
	ds_read_b128 v[60:63], v153 offset:53248
	v_add_u32_e32 v113, 0, v147
	s_waitcnt lgkmcnt(5)
	v_mfma_f32_32x32x16_bf16 v[32:47], v[0:3], v[104:107], 0
	v_bitop3_b32 v157, v112, v4, s60 bitop3:0x36
	v_add_u32_e32 v156, v152, v157
	ds_read_b128 v[64:67], v156 offset:49152
	ds_read_b128 v[68:71], v156 offset:53248
	s_mov_b32 s68, s69
	s_mov_b32 s70, s69
	s_mov_b32 s71, s69
	s_mov_b32 s72, s69
	s_waitcnt lgkmcnt(6)
	v_mfma_f32_32x32x16_bf16 v[16:31], v[16:19], v[104:107], 0
	s_mov_b32 s73, s69
	s_mov_b32 s74, s69
	s_mov_b32 s75, s69
	s_mov_b32 s76, s69
	s_mov_b32 s77, s69
	s_mov_b32 s78, s69
	s_mov_b32 s79, s69
	s_mov_b32 s80, s69
	s_mov_b32 s81, s69
	s_mov_b32 s82, s69
	s_mov_b32 s83, s69
	v_mov_b64_e32 v[0:1], s[68:69]
	v_mov_b64_e32 v[2:3], s[70:71]
	v_mov_b64_e32 v[4:5], s[72:73]
	v_mov_b64_e32 v[6:7], s[74:75]
	v_mov_b64_e32 v[8:9], s[76:77]
	v_mov_b64_e32 v[10:11], s[78:79]
	v_mov_b64_e32 v[12:13], s[80:81]
	v_mov_b64_e32 v[14:15], s[82:83]
	s_waitcnt lgkmcnt(5)
	v_mfma_f32_32x32x16_bf16 v[32:47], v[48:51], v[108:111], v[32:47]
	s_waitcnt lgkmcnt(4)
	v_mfma_f32_32x32x16_bf16 v[16:31], v[52:55], v[108:111], v[16:31]
	s_waitcnt lgkmcnt(3)
	v_mfma_f32_32x32x16_bf16 v[32:47], v[56:59], v[100:103], v[32:47]
	s_waitcnt lgkmcnt(2)
	v_mfma_f32_32x32x16_bf16 v[16:31], v[60:63], v[100:103], v[16:31]
	s_waitcnt lgkmcnt(1)
	v_mfma_f32_32x32x16_bf16 v[32:47], v[64:67], v[96:99], v[32:47]
	s_waitcnt lgkmcnt(0)
	v_mfma_f32_32x32x16_bf16 v[16:31], v[68:71], v[96:99], v[16:31]
	s_nop 9
	v_max_f32_e32 v48, v33, v33
	v_max_f32_e32 v49, v32, v32
	v_max_f32_e32 v48, v49, v48
	v_max3_f32 v48, v48, v34, v35
	v_max3_f32 v48, v48, v36, v37
	v_max3_f32 v48, v48, v38, v39
	v_max3_f32 v48, v48, v40, v41
	v_max3_f32 v48, v48, v42, v43
	v_max3_f32 v48, v48, v44, v45
	v_max3_f32 v48, v48, v46, v47
	v_max3_f32 v48, v48, v16, v17
	v_max3_f32 v48, v48, v18, v19
	v_max3_f32 v48, v48, v20, v21
	v_max3_f32 v48, v48, v22, v23
	v_max3_f32 v48, v48, v24, v25
	v_max3_f32 v48, v48, v26, v27
	v_max3_f32 v48, v48, v28, v29
	v_max3_f32 v48, v48, v30, v31
	v_mov_b32_e32 v49, v48
	s_nop 1
	v_permlane32_swap_b32_e32 v48, v49
	v_max_f32_e32 v49, v49, v49
	v_max_f32_e32 v48, v48, v48
	v_max_f32_e32 v48, v48, v49
	v_add_f32_e32 v49, 0x7149f2ca, v48
	s_mov_b32 s19, 0x42800000
	v_max_f32_e32 v48, 0xf149f2ca, v48
	v_cmp_ge_f32_e32 vcc, s19, v49
	v_sub_f32_e32 v49, 0xf149f2ca, v48
	v_mul_f32_e32 v49, 0x3e38aa3b, v49
	v_exp_f32_e32 v49, v49
	s_cmp_eq_u64 vcc, exec
	s_cselect_b64 vcc, -1, 0
	v_cndmask_b32_e32 v159, v48, v220, vcc
	v_mul_f32_e32 v48, 0xbe38aa3b, v159
	v_cndmask_b32_e64 v158, v49, 1.0, vcc
	v_mov_b32_e32 v49, v48
	v_fmamk_f32 v32, v32, 0x3e38aa3b, v48
	v_fmamk_f32 v33, v33, 0x3e38aa3b, v48
	v_fmamk_f32 v34, v34, 0x3e38aa3b, v48
	v_fmamk_f32 v35, v35, 0x3e38aa3b, v48
	v_fmamk_f32 v36, v36, 0x3e38aa3b, v48
	v_fmamk_f32 v37, v37, 0x3e38aa3b, v48
	v_fmamk_f32 v38, v38, 0x3e38aa3b, v48
	v_fmamk_f32 v39, v39, 0x3e38aa3b, v48
	v_fmamk_f32 v40, v40, 0x3e38aa3b, v48
	v_fmamk_f32 v41, v41, 0x3e38aa3b, v48
	v_fmamk_f32 v42, v42, 0x3e38aa3b, v48
	v_fmamk_f32 v43, v43, 0x3e38aa3b, v48
	v_fmamk_f32 v44, v44, 0x3e38aa3b, v48
	v_fmamk_f32 v45, v45, 0x3e38aa3b, v48
	v_fmamk_f32 v46, v46, 0x3e38aa3b, v48
	v_fmac_f32_e32 v49, 0x3e38aa3b, v47
	v_exp_f32_e32 v173, v32
	v_exp_f32_e32 v175, v33
	v_exp_f32_e32 v171, v34
	v_exp_f32_e32 v174, v35
	v_exp_f32_e32 v169, v36
	v_exp_f32_e32 v172, v37
	v_exp_f32_e32 v168, v38
	v_exp_f32_e32 v170, v39
	v_exp_f32_e32 v165, v40
	v_exp_f32_e32 v167, v41
	v_exp_f32_e32 v163, v42
	v_exp_f32_e32 v166, v43
	v_exp_f32_e32 v161, v44
	v_exp_f32_e32 v164, v45
	v_exp_f32_e32 v160, v46
	v_exp_f32_e32 v162, v49
	v_pk_fma_f32 v[124:125], v[30:31], s[92:93], v[48:49] op_sel_hi:[1,0,0]
	v_pk_fma_f32 v[126:127], v[28:29], s[92:93], v[48:49] op_sel_hi:[1,0,0]
	v_pk_fma_f32 v[128:129], v[26:27], s[92:93], v[48:49] op_sel_hi:[1,0,0]
	v_pk_fma_f32 v[130:131], v[24:25], s[92:93], v[48:49] op_sel_hi:[1,0,0]
	v_pk_fma_f32 v[132:133], v[22:23], s[92:93], v[48:49] op_sel_hi:[1,0,0]
	v_pk_fma_f32 v[134:135], v[20:21], s[92:93], v[48:49] op_sel_hi:[1,0,0]
	v_pk_fma_f32 v[136:137], v[18:19], s[92:93], v[48:49] op_sel_hi:[1,0,0]
	v_pk_fma_f32 v[138:139], v[16:17], s[92:93], v[48:49] op_sel_hi:[1,0,0]
	v_mov_b64_e32 v[62:63], v[14:15]
	v_mov_b64_e32 v[46:47], v[14:15]
	v_mov_b64_e32 v[30:31], v[14:15]
	v_cmp_gt_u32_e64 s[2:3], 32, v72
	v_lshl_add_u32 v145, v141, 2, v144
	v_or3_b32 v114, v75, v73, v74
	v_mov_b32_e32 v115, v193
	v_or3_b32 v116, v76, v73, v74
	v_mov_b32_e32 v117, v193
	v_mov_b32_e32 v146, 0
	s_mov_b32 s18, -1
	v_mov_b64_e32 v[60:61], v[12:13]
	v_mov_b64_e32 v[58:59], v[10:11]
	v_mov_b64_e32 v[56:57], v[8:9]
	v_mov_b64_e32 v[54:55], v[6:7]
	v_mov_b64_e32 v[52:53], v[4:5]
	v_mov_b64_e32 v[50:51], v[2:3]
	v_mov_b64_e32 v[48:49], v[0:1]
	v_mov_b64_e32 v[44:45], v[12:13]
	v_mov_b64_e32 v[42:43], v[10:11]
	v_mov_b64_e32 v[40:41], v[8:9]
	v_mov_b64_e32 v[38:39], v[6:7]
	v_mov_b64_e32 v[36:37], v[4:5]
	v_mov_b64_e32 v[34:35], v[2:3]
	v_mov_b64_e32 v[32:33], v[0:1]
	v_mov_b64_e32 v[28:29], v[12:13]
	v_mov_b64_e32 v[26:27], v[10:11]
	v_mov_b64_e32 v[24:25], v[8:9]
	v_mov_b64_e32 v[22:23], v[6:7]
	v_mov_b64_e32 v[20:21], v[4:5]
	v_mov_b64_e32 v[18:19], v[2:3]
	v_mov_b64_e32 v[16:17], v[0:1]
	s_mov_b64 s[22:23], 0x2901c00
	s_mov_b64 s[24:25], 0x2981c00
; #define LAS __attribute__((address_space(3)))
; __device__ __forceinline__ float clamp8(float x) { return __builtin_amdgcn_fmed3f(x, -448.f, 448.f); }
; #define VM_WAIT() asm volatile("s_waitcnt vmcnt(0)" ::: "memory")
;     ...
;         f32x16 pB0, pB1; float mnB, alB;
;         GLDS3(0); GLDS3(1); VM_WAIT(); __syncthreads();
;         qkt<MODE>(p0, p1, KB3(0), qr, r32, hi); partialSM<MODE>(p0, p1, m_reg, mn, al);
; #pragma unroll 1
;         for (int j = 1; j + 1 < NT; j += 2) {
;             GLDS3(j + 1);
; __device__ __forceinline__ void cvt_finish(const CvtDesc& d, const float (&t)[64], LAS float* scr, int lane) {
;     ...
;     if (d.f8) {
; #pragma unroll
;         for (int j = 0; j < 8; ++j) { const int n = (lane >> 3) + 8 * j; const LAS float* s = scr + (8 * c) * 65 + n;
;             int a = __builtin_amdgcn_cvt_pk_fp8_f32(clamp8(s[0 * 65] * W8_SCALE), clamp8(s[1 * 65] * W8_SCALE), 0, false); a = __builtin_amdgcn_cvt_pk_fp8_f32(clamp8(s[2 * 65] * W8_SCALE), clamp8(s[3 * 65] * W8_SCALE), a, true);
;             int b = __builtin_amdgcn_cvt_pk_fp8_f32(clamp8(s[4 * 65] * W8_SCALE), clamp8(s[5 * 65] * W8_SCALE), 0, false); b = __builtin_amdgcn_cvt_pk_fp8_f32(clamp8(s[6 * 65] * W8_SCALE), clamp8(s[7 * 65] * W8_SCALE), b, true);
;             __builtin_nontemporal_store((u32x2){(unsigned)a, (unsigned)b}, (u32x2*)(d.dst + (size_t)n * d.dKB + 8 * c)); }
.LBB0_487:
	s_mul_i32 s0, s18, 0xab
	s_addk_i32 s0, 0x201
	s_bfe_u32 s0, s0, 0x70009
	s_mul_i32 s0, s0, 3
	s_sub_i32 s0, s18, s0
	s_add_i32 s0, s0, 3
	s_and_b32 s0, s0, 0xff
	s_lshl_b32 s1, s0, 14
	s_mulk_i32 s0, 0x6000
	s_add_i32 s1, s14, s1
	s_add_i32 s17, s0, 0
	v_lshl_add_u64 v[118:119], s[6:7], 0, v[114:115]
	s_add_i32 s0, s17, s13
	v_lshl_add_u64 v[64:65], v[118:119], 0, s[22:23]
	s_mov_b32 m0, s1
	v_lshl_add_u64 v[120:121], s[6:7], 0, v[116:117]
	s_add_i32 s4, s0, 0xc000
	global_load_lds_dwordx4 v[64:65], off
	v_lshl_add_u64 v[64:65], v[120:121], 0, s[22:23]
	s_add_i32 m0, s1, 0x2000
	v_lshl_add_u64 v[122:123], s[6:7], 0, v[192:193]
	s_mov_b64 s[0:1], 0x2901880
	global_load_lds_dwordx4 v[64:65], off
	v_lshl_add_u64 v[64:65], v[122:123], 0, s[0:1]
	s_mov_b32 m0, s4
	s_add_i32 s15, s18, 2
	global_load_lds_dwordx4 v[64:65], off
	s_add_u32 s52, s52, 16
	s_cmp_ge_u32 s52, 31
	s_cselect_b32 s50, 1, 0
	s_cbranch_scc0 .Lilc_n_da
	s_sub_u32 s52, s52, 31
	s_mov_b32 s46, s51
	s_add_u32 s51, s51, 1
	s_lshl_b32 s49, s46, 2
	s_add_u32 s49, s49, s54
	s_cmp_lt_u32 s49, 0xc3
	s_cselect_b32 s50, 1, 0
	s_cbranch_scc0 .Lilc_n_da
	s_lshr_b32 s55, s46, 4
	s_and_b32 s57, s49, 63
	s_lshl_b32 s101, s56, 6
	s_add_u32 s101, s101, s57
	s_cmp_eq_u32 s55, 3
	s_cselect_b32 s55, s54, s55
	s_cselect_b32 s100, 3, 0
	s_cselect_b32 s101, s56, s101
	s_cselect_b32 s57, 64, s57
	s_add_u32 s100, s100, s55
	s_lshl_b32 s100, s100, 3
	s_add_u32 s100, s100, 0xa0
	s_load_dwordx2 s[44:45], s[36:37], s100
.Lilc_n_da:
	s_cmp_eq_u32 s42, 0
	s_cbranch_scc1 .Lilc_np_da
	s_mov_b32 s53, 4
	v_mul_f32_e32 v232, 0x42800000, v232
	v_mul_f32_e32 v233, 0x42800000, v233
	v_mul_f32_e32 v234, 0x42800000, v234
	v_mul_f32_e32 v235, 0x42800000, v235
	v_mul_f32_e32 v236, 0x42800000, v236
	v_mul_f32_e32 v237, 0x42800000, v237
	v_mul_f32_e32 v238, 0x42800000, v238
	v_mul_f32_e32 v239, 0x42800000, v239
	v_mul_f32_e32 v240, 0x42800000, v240
	v_mul_f32_e32 v241, 0x42800000, v241
	v_mul_f32_e32 v242, 0x42800000, v242
	v_mul_f32_e32 v243, 0x42800000, v243
	v_mul_f32_e32 v244, 0x42800000, v244
	v_mul_f32_e32 v245, 0x42800000, v245
	v_mul_f32_e32 v246, 0x42800000, v246
	v_mul_f32_e32 v247, 0x42800000, v247
	v_mul_f32_e32 v248, 0x42800000, v248
	v_mul_f32_e32 v249, 0x42800000, v249
	v_mul_f32_e32 v250, 0x42800000, v250
	v_mul_f32_e32 v251, 0x42800000, v251
	v_mul_f32_e32 v206, 0x42800000, v206
	v_mul_f32_e32 v207, 0x42800000, v207
	v_mul_f32_e32 v208, 0x42800000, v208
	v_mul_f32_e32 v209, 0x42800000, v209
	v_mul_f32_e32 v210, 0x42800000, v210
	v_mul_f32_e32 v211, 0x42800000, v211
	v_mul_f32_e32 v212, 0x42800000, v212
	v_mul_f32_e32 v213, 0x42800000, v213
	v_mul_f32_e32 v214, 0x42800000, v214
	v_mul_f32_e32 v215, 0x42800000, v215
	v_mul_f32_e32 v216, 0x42800000, v216
	v_mul_f32_e32 v217, 0x42800000, v217
	v_med3_f32 v232, v232, s93, v224
	v_med3_f32 v233, v233, s93, v224
	v_med3_f32 v234, v234, s93, v224
	v_med3_f32 v235, v235, s93, v224
	v_med3_f32 v236, v236, s93, v224
	v_med3_f32 v237, v237, s93, v224
	v_med3_f32 v238, v238, s93, v224
	v_med3_f32 v239, v239, s93, v224
	v_med3_f32 v240, v240, s93, v224
	v_med3_f32 v241, v241, s93, v224
	v_med3_f32 v242, v242, s93, v224
	v_med3_f32 v243, v243, s93, v224
	v_med3_f32 v244, v244, s93, v224
	v_med3_f32 v245, v245, s93, v224
	v_med3_f32 v246, v246, s93, v224
	v_med3_f32 v247, v247, s93, v224
	v_med3_f32 v248, v248, s93, v224
	v_med3_f32 v249, v249, s93, v224
	v_med3_f32 v250, v250, s93, v224
	v_med3_f32 v251, v251, s93, v224
	v_med3_f32 v206, v206, s93, v224
	v_med3_f32 v207, v207, s93, v224
	v_med3_f32 v208, v208, s93, v224
	v_med3_f32 v209, v209, s93, v224
	v_med3_f32 v210, v210, s93, v224
	v_med3_f32 v211, v211, s93, v224
	v_med3_f32 v212, v212, s93, v224
	v_med3_f32 v213, v213, s93, v224
	v_med3_f32 v214, v214, s93, v224
	v_med3_f32 v215, v215, s93, v224
	v_med3_f32 v216, v216, s93, v224
	v_med3_f32 v217, v217, s93, v224
	v_lshlrev_b32_e32 v230, 3, v226
	v_lshl_add_u32 v225, v229, s42, v230
	v_cvt_pk_fp8_f32 v252, v232, v236
	v_cvt_pk_fp8_f32 v253, v248, v206
	v_cvt_pk_fp8_f32 v252, v240, v244 op_sel:[0,0,1]
	v_cvt_pk_fp8_f32 v253, v210, v214 op_sel:[0,0,1]
	s_nop 0
	global_store_dwordx2 v225, v[252:253], s[40:41]
	v_add_u32_e32 v225, s43, v225
	v_cvt_pk_fp8_f32 v252, v233, v237
	v_cvt_pk_fp8_f32 v253, v249, v207
	v_cvt_pk_fp8_f32 v252, v241, v245 op_sel:[0,0,1]
	v_cvt_pk_fp8_f32 v253, v211, v215 op_sel:[0,0,1]
	s_nop 0
	global_store_dwordx2 v225, v[252:253], s[40:41]
	v_add_u32_e32 v225, s43, v225
	v_cvt_pk_fp8_f32 v252, v234, v238
	v_cvt_pk_fp8_f32 v253, v250, v208
	v_cvt_pk_fp8_f32 v252, v242, v246 op_sel:[0,0,1]
	v_cvt_pk_fp8_f32 v253, v212, v216 op_sel:[0,0,1]
	s_nop 0
	global_store_dwordx2 v225, v[252:253], s[40:41]
	v_add_u32_e32 v225, s43, v225
	v_cvt_pk_fp8_f32 v252, v235, v239
	v_cvt_pk_fp8_f32 v253, v251, v209
	v_cvt_pk_fp8_f32 v252, v243, v247 op_sel:[0,0,1]
	v_cvt_pk_fp8_f32 v253, v213, v217 op_sel:[0,0,1]
	s_nop 0
	global_store_dwordx2 v225, v[252:253], s[40:41]
	s_mov_b32 s42, 0
	s_branch .Lilc_i_da
.Lilc_np_da:
	s_mov_b32 s53, 0
.Lilc_i_da:
	s_cmp_eq_u32 s50, 0
	s_cbranch_scc1 .Lilc_d_da
	s_waitcnt lgkmcnt(0)
	s_lshr_b32 s49, s101, 10
	s_lshl_b32 s101, s101, 22
	s_add_u32 s44, s44, s101
	s_addc_u32 s45, s45, s49
	s_cmp_eq_u32 s55, 2
	s_cbranch_scc1 .Lilc_dn_da
	s_lshr_b32 s49, s39, 4
	s_and_b32 s46, s39, 15
	s_lshl_b32 s100, s49, 17
	s_lshl_b32 s101, s46, 7
	s_add_u32 s100, s100, s101
	s_add_u32 s44, s44, s100
	s_addc_u32 s45, s45, 0
	s_lshr_b32 s100, s46, 2
	s_lshl_b32 s100, s100, 8
	s_lshl_b32 s101, s55, 7
	s_add_u32 s100, s100, s101
	s_and_b32 s101, s46, 3
	s_lshl_b32 s101, s101, 5
	s_add_u32 s100, s100, s101
	s_lshl_b32 s100, s100, 11
	s_lshl_b32 s101, s49, 6
	s_add_u32 s100, s100, s101
	s_lshl_b32 s101, s57, 21
	s_add_u32 s100, s100, s101
	s_add_u32 s100, s100, 0x34000000
	s_mul_i32 s101, s56, 0x1a800000
	s_add_u32 s100, s100, s101
	s_add_u32 s40, s34, s100
	s_addc_u32 s41, s35, 0
	s_mov_b32 s42, 13
	s_movk_i32 s43, 0x800
	s_movk_i32 s47, 0x800
	s_mov_b32 s48, 14
	s_branch .Lilc_is_da
; #define SBAR() __builtin_amdgcn_sched_barrier(0)
;     __device__ __forceinline__ const float* in(int i) const { return *(const float* const __attribute__((address_space(4)))*)(p + 8 * i); }
;     __device__ __forceinline__ unsigned char* ws() const { return *(unsigned char* const __attribute__((address_space(4)))*)(p + 232); }
;     ...
;             SBAR(); qkt<MODE>(pB0, pB1, KB3(j), qr, r32, hi);
;             finishSM(p0, p1, al, l_reg, pa0, pa1, pa2, pa3); SBAR();
;             pv_d0(o, VB3(j - 1), pa0, pa1, pa2, pa3); partialSM<MODE>(pB0, pB1, m_reg, mnB, alB);
; __device__ __forceinline__ CvtDesc conv_expert_desc(const KA& a, unsigned char* ws, int q) {
;     const int l = q / Q_PER_L; int r = q - l * Q_PER_L;
;     unsigned char* wl = ws + WS_W + (size_t)l * W_LSTRIDE;
;     CvtDesc d; d.f8 = (MOE_FP8_LAST && (MOE_FP8_GU_ALL || l == NLAYER - 1)) ? 1 : 0;
;     if (MOE_FP8_LAST && MOE_FP8_DOWN_ALL && r >= 2 * Q_IG) d.f8 = 1;
;     const int eb = d.f8 ? 1 : 2;
;     if (r < 2 * Q_IG) { const int up = r >= Q_IG; if (up) r -= Q_IG; const int e = r >> 8, rr = r & 255, kb = rr >> 3, nb = rr & 7, n0 = nb * 64;
;         const float* src = e < 64 ? a.in(up ? 21 : 20) + ((size_t)l * 64 + e) * DM * FFE : a.in(up ? 24 : 23) + (size_t)l * DM * FFE;
;         d.src = src + (size_t)(kb * 64) * FFE + n0; d.N = FFE; d.dKB = DM * eb;
;         d.dst = wl + W_GU + ((size_t)e * 1024 * DM + (size_t)((n0 >> 7) * 256 + up * 128 + (n0 & 127)) * DM + kb * 64) * eb;
;     } else { r -= 2 * Q_IG; const int e = r >> 8, rr = r & 255, kb = rr >> 5, nb = rr & 31;
;         const float* src = e < 64 ? a.in(22) + ((size_t)l * 64 + e) * FFE * DM : a.in(25) + (size_t)l * FFE * DM;
;         d.src = src + (size_t)(kb * 64) * DM + nb * 64; d.N = DM; d.dKB = FFE * eb;
;         d.dst = wl + W_D + ((size_t)e * DM * FFE + (size_t)(nb * 64) * FFE + kb * 64) * eb; }
.Lilc_dn_da:
	s_lshr_b32 s49, s39, 6
	s_and_b32 s46, s39, 63
	s_lshl_b32 s100, s49, 19
	s_lshl_b32 s101, s46, 7
	s_add_u32 s100, s100, s101
	s_add_u32 s44, s44, s100
	s_addc_u32 s45, s45, 0
	s_lshl_b32 s100, s46, 14
	s_lshl_b32 s101, s49, 6
	s_add_u32 s100, s100, s101
	s_lshl_b32 s101, s57, 20
	s_add_u32 s100, s100, s101
	s_add_u32 s100, s100, 0x44400000
	s_mul_i32 s101, s56, 0x1a800000
	s_add_u32 s100, s100, s101
	s_add_u32 s40, s34, s100
	s_addc_u32 s41, s35, 0
	s_mov_b32 s42, 11
	s_movk_i32 s43, 0x200
	s_movk_i32 s47, 0x2000
	s_mov_b32 s48, 16
.Lilc_is_da:
	s_add_u32 s53, s53, 8
	v_lshlrev_b32_e32 v230, 4, v229
	v_lshl_add_u32 v223, v226, s48, v230
	global_load_dwordx4 v[232:235], v223, s[44:45] nt
	v_add_u32_e32 v223, s47, v223
	global_load_dwordx4 v[236:239], v223, s[44:45] nt
	v_add_u32_e32 v223, s47, v223
	global_load_dwordx4 v[240:243], v223, s[44:45] nt
	v_add_u32_e32 v223, s47, v223
	global_load_dwordx4 v[244:247], v223, s[44:45] nt
	v_add_u32_e32 v223, s47, v223
	global_load_dwordx4 v[248:251], v223, s[44:45] nt
	v_add_u32_e32 v223, s47, v223
	global_load_dwordx4 v[206:209], v223, s[44:45] nt
	v_add_u32_e32 v223, s47, v223
	global_load_dwordx4 v[210:213], v223, s[44:45] nt
	v_add_u32_e32 v223, s47, v223
	global_load_dwordx4 v[214:217], v223, s[44:45] nt
.Lilc_d_da:
	s_mul_i32 s0, s15, 0xab
	s_bfe_u32 s0, s0, 0x70009
	s_mul_i32 s0, s0, 3
	s_sub_i32 s0, s15, s0
	s_and_b32 s16, s0, 0xff
	s_mul_i32 s0, s16, 0x6000
	v_add_u32_e32 v72, s0, v152
	v_add_u32_e32 v68, v72, v150
	v_add_u32_e32 v73, v72, v154
	ds_read_b128 v[64:67], v68 offset:49152
	ds_read_b128 v[68:71], v68 offset:53248
	ds_read_b128 v[176:179], v73 offset:49152
	ds_read_b128 v[180:183], v73 offset:53248
	v_add_u32_e32 v73, v72, v155
	ds_read_b128 v[184:187], v73 offset:49152
	ds_read_b128 v[188:191], v73 offset:53248
	s_waitcnt lgkmcnt(0)
	v_mfma_f32_32x32x16_bf16 v[80:95], v[64:67], v[104:107], 0
	v_add_u32_e32 v64, v72, v157
	ds_read_b128 v[194:197], v64 offset:49152
	ds_read_b128 v[198:201], v64 offset:53248
	v_mfma_f32_32x32x16_bf16 v[64:79], v[68:71], v[104:107], 0
	v_mfma_f32_32x32x16_bf16 v[80:95], v[176:179], v[108:111], v[80:95]
	v_mfma_f32_32x32x16_bf16 v[64:79], v[180:183], v[108:111], v[64:79]
	v_mfma_f32_32x32x16_bf16 v[80:95], v[184:187], v[100:103], v[80:95]
	v_mfma_f32_32x32x16_bf16 v[64:79], v[188:191], v[100:103], v[64:79]
	s_waitcnt lgkmcnt(0)
	v_mfma_f32_32x32x16_bf16 v[80:95], v[194:197], v[96:99], v[80:95]
	v_mfma_f32_32x32x16_bf16 v[64:79], v[198:201], v[96:99], v[64:79]
	v_exp_f32_e32 v186, v124
	v_add_f32_e32 v124, 0, v173
	v_add_f32_e32 v124, v175, v124
	v_add_f32_e32 v124, v171, v124
	v_add_f32_e32 v124, v174, v124
	v_add_f32_e32 v124, v169, v124
	v_add_f32_e32 v124, v172, v124
	v_add_f32_e32 v124, v168, v124
	v_add_f32_e32 v124, v170, v124
	v_add_f32_e32 v124, v165, v124
	v_add_f32_e32 v124, v167, v124
	v_add_f32_e32 v124, v163, v124
	v_add_f32_e32 v124, v166, v124
	v_exp_f32_e32 v138, v138
	v_add_f32_e32 v124, v161, v124
	v_exp_f32_e32 v139, v139
	v_add_f32_e32 v124, v164, v124
	v_exp_f32_e32 v136, v136
	v_add_f32_e32 v124, v160, v124
	v_exp_f32_e32 v137, v137
	v_add_f32_e32 v124, v162, v124
	v_exp_f32_e32 v176, v134
	v_add_f32_e32 v124, v138, v124
	v_exp_f32_e32 v177, v135
	v_add_f32_e32 v124, v139, v124
	v_exp_f32_e32 v178, v132
	v_add_f32_e32 v124, v136, v124
	v_exp_f32_e32 v179, v133
	v_add_f32_e32 v124, v137, v124
	v_exp_f32_e32 v180, v130
	v_add_f32_e32 v124, v176, v124
	v_exp_f32_e32 v181, v131
	v_add_f32_e32 v124, v177, v124
	v_exp_f32_e32 v182, v128
	v_add_f32_e32 v124, v178, v124
	v_exp_f32_e32 v183, v129
	v_add_f32_e32 v124, v179, v124
	v_exp_f32_e32 v184, v126
	v_add_f32_e32 v124, v180, v124
	v_exp_f32_e32 v185, v127
	v_add_f32_e32 v124, v181, v124
	v_add_f32_e32 v124, v182, v124
	v_exp_f32_e32 v187, v125
	v_add_f32_e32 v124, v183, v124
	v_add_f32_e32 v124, v184, v124
	v_add_f32_e32 v124, v185, v124
	v_add_f32_e32 v124, v186, v124
	v_add_f32_e32 v124, v187, v124
	v_mov_b32_e32 v125, v124
	v_cvt_pk_bf16_f32 v126, v173, v175
	v_cvt_pk_bf16_f32 v127, v171, v174
	v_cvt_pk_bf16_f32 v128, v169, v172
	v_cvt_pk_bf16_f32 v129, v168, v170
	s_nop 1
	v_permlane32_swap_b32_e32 v124, v125
	v_permlane32_swap_b32_e32 v126, v128
	v_permlane32_swap_b32_e32 v127, v129
	v_cvt_pk_bf16_f32 v130, v165, v167
	v_cvt_pk_bf16_f32 v131, v163, v166
	v_cvt_pk_bf16_f32 v132, v161, v164
	v_cvt_pk_bf16_f32 v133, v160, v162
	v_cvt_pk_bf16_f32 v134, v138, v139
	v_cvt_pk_bf16_f32 v135, v136, v137
	v_cvt_pk_bf16_f32 v136, v176, v177
	v_cvt_pk_bf16_f32 v137, v178, v179
	v_cvt_pk_bf16_f32 v160, v180, v181
	v_cvt_pk_bf16_f32 v161, v182, v183
	v_cvt_pk_bf16_f32 v162, v184, v185
	v_cvt_pk_bf16_f32 v163, v186, v187
	s_nop 0
	v_permlane32_swap_b32_e32 v130, v132
	v_permlane32_swap_b32_e32 v131, v133
	v_permlane32_swap_b32_e32 v134, v136
	v_permlane32_swap_b32_e32 v135, v137
	v_permlane32_swap_b32_e32 v160, v162
	v_permlane32_swap_b32_e32 v161, v163
	s_add_i32 s0, s18, 0x10001
	s_and_b32 s1, s0, 0xff
	s_mulk_i32 s1, 0xab
	s_bfe_u32 s1, s1, 0x70009
	s_mul_i32 s1, s1, 3
	s_sub_i32 s0, s0, s1
	s_and_b32 s0, s0, 0xff
	v_lshl_add_u32 v138, s0, 14, v113
	ds_read_b64_tr_b16 v[164:165], v138 offset:0
	ds_read_b64_tr_b16 v[166:167], v138 offset:0x800
	ds_read_b64_tr_b16 v[168:169], v138 offset:0x1000
	ds_read_b64_tr_b16 v[170:171], v138 offset:0x1800
	ds_read_b64_tr_b16 v[172:173], v138 offset:0x2000
	ds_read_b64_tr_b16 v[174:175], v138 offset:0x2800
	ds_read_b64_tr_b16 v[176:177], v138 offset:0x3000
	ds_read_b64_tr_b16 v[178:179], v138 offset:0x3800
	s_waitcnt lgkmcnt(0)
; #define VM_WAIT() asm volatile("s_waitcnt vmcnt(0)" ::: "memory")
; #define SBAR() __builtin_amdgcn_sched_barrier(0)
; #define RESC(a) do { if (__any((a) < 1.f)) { if (hi == 0) al_l[r32] = (a); asm volatile("s_waitcnt lgkmcnt(0)" ::: "memory"); \
;         _Pragma("unroll") for (int d = 0; d < 4; ++d) _Pragma("unroll") for (int r = 0; r < 16; ++r) o[d][r] *= al_l[crow(r, hi)]; } } while (0)
; template <int D0> __device__ __forceinline__ void pv_one(f32x16& od, int vb, bf16x8 pa0, bf16x8 pa1, bf16x8 pa2, bf16x8 pa3) {
;     const s16x4 l0 = tr_read<v_rd_off(D0, 0, 0)>(vb), h0 = tr_read<v_rd_off(D0, 0, 1)>(vb), l1 = tr_read<v_rd_off(D0, 1, 0)>(vb), h1 = tr_read<v_rd_off(D0, 1, 1)>(vb);
;     const s16x4 l2 = tr_read<v_rd_off(D0, 2, 0)>(vb), h2 = tr_read<v_rd_off(D0, 2, 1)>(vb), l3 = tr_read<v_rd_off(D0, 3, 0)>(vb), h3 = tr_read<v_rd_off(D0, 3, 1)>(vb);
;     asm volatile("s_waitcnt lgkmcnt(0)" ::: "memory"); SBAR();
;     ...
;     od = __builtin_amdgcn_mfma_f32_32x32x16_bf16(pa0, PK(l0, h0), od, 0, 0, 0);
;     od = __builtin_amdgcn_mfma_f32_32x32x16_bf16(pa1, PK(l1, h1), od, 0, 0, 0);
;     od = __builtin_amdgcn_mfma_f32_32x32x16_bf16(pa2, PK(l2, h2), od, 0, 0, 0);
;     od = __builtin_amdgcn_mfma_f32_32x32x16_bf16(pa3, PK(l3, h3), od, 0, 0, 0);
;     ...
; }
; __device__ __forceinline__ void pv_d0(f32x16* o, int vb, bf16x8 pa0, bf16x8 pa1, bf16x8 pa2, bf16x8 pa3) {
;     pv_one<0>(o[0], vb, pa0, pa1, pa2, pa3); pv_one<1>(o[1], vb, pa0, pa1, pa2, pa3); pv_one<2>(o[2], vb, pa0, pa1, pa2, pa3); pv_one<3>(o[3], vb, pa0, pa1, pa2, pa3);
; }
;     ...
;             pv_d0(o, VB3(j - 1), pa0, pa1, pa2, pa3); partialSM<MODE>(pB0, pB1, m_reg, mnB, alB);
;             RESC(alB); VM_WAIT(); __syncthreads();
	s_nop 0
	v_mfma_f32_32x32x16_bf16 v[0:15], v[126:129], v[164:167], v[0:15]
	ds_read_b64_tr_b16 v[164:165], v138 offset:0x200
	ds_read_b64_tr_b16 v[166:167], v138 offset:0xa00
	v_mfma_f32_32x32x16_bf16 v[0:15], v[130:133], v[168:171], v[0:15]
	ds_read_b64_tr_b16 v[168:169], v138 offset:0x1200
	ds_read_b64_tr_b16 v[170:171], v138 offset:0x1a00
	v_mfma_f32_32x32x16_bf16 v[0:15], v[134:137], v[172:175], v[0:15]
	ds_read_b64_tr_b16 v[172:173], v138 offset:0x2200
	ds_read_b64_tr_b16 v[174:175], v138 offset:0x2a00
	v_mfma_f32_32x32x16_bf16 v[0:15], v[160:163], v[176:179], v[0:15]
	ds_read_b64_tr_b16 v[176:177], v138 offset:0x3200
	ds_read_b64_tr_b16 v[178:179], v138 offset:0x3a00
	s_waitcnt lgkmcnt(0)
	v_mfma_f32_32x32x16_bf16 v[48:63], v[126:129], v[164:167], v[48:63]
	ds_read_b64_tr_b16 v[164:165], v138 offset:0x400
	ds_read_b64_tr_b16 v[166:167], v138 offset:0xc00
	v_mfma_f32_32x32x16_bf16 v[48:63], v[130:133], v[168:171], v[48:63]
	ds_read_b64_tr_b16 v[168:169], v138 offset:0x1400
	ds_read_b64_tr_b16 v[170:171], v138 offset:0x1c00
	v_mfma_f32_32x32x16_bf16 v[48:63], v[134:137], v[172:175], v[48:63]
	ds_read_b64_tr_b16 v[172:173], v138 offset:0x2400
	ds_read_b64_tr_b16 v[174:175], v138 offset:0x2c00
	v_mfma_f32_32x32x16_bf16 v[48:63], v[160:163], v[176:179], v[48:63]
	ds_read_b64_tr_b16 v[176:177], v138 offset:0x3400
	ds_read_b64_tr_b16 v[178:179], v138 offset:0x3c00
	s_waitcnt lgkmcnt(0)
	v_mfma_f32_32x32x16_bf16 v[32:47], v[126:129], v[164:167], v[32:47]
	ds_read_b64_tr_b16 v[164:165], v138 offset:0x600
	ds_read_b64_tr_b16 v[166:167], v138 offset:0xe00
	v_mfma_f32_32x32x16_bf16 v[32:47], v[130:133], v[168:171], v[32:47]
	ds_read_b64_tr_b16 v[168:169], v138 offset:0x1600
	ds_read_b64_tr_b16 v[170:171], v138 offset:0x1e00
	v_mfma_f32_32x32x16_bf16 v[32:47], v[134:137], v[172:175], v[32:47]
	ds_read_b64_tr_b16 v[172:173], v138 offset:0x2600
	ds_read_b64_tr_b16 v[174:175], v138 offset:0x2e00
	v_mfma_f32_32x32x16_bf16 v[32:47], v[160:163], v[176:179], v[32:47]
	ds_read_b64_tr_b16 v[176:177], v138 offset:0x3600
	ds_read_b64_tr_b16 v[178:179], v138 offset:0x3e00
	s_waitcnt lgkmcnt(0)
	v_mfma_f32_32x32x16_bf16 v[16:31], v[126:129], v[164:167], v[16:31]
	v_max_f32_e32 v126, v81, v81
	v_max_f32_e32 v127, v80, v80
	v_max_f32_e32 v126, v127, v126
	v_max3_f32 v126, v126, v82, v83
	v_max3_f32 v126, v126, v84, v85
	v_max3_f32 v126, v126, v86, v87
	v_max3_f32 v126, v126, v88, v89
	v_max3_f32 v126, v126, v90, v91
	v_max3_f32 v126, v126, v92, v93
	v_mfma_f32_32x32x16_bf16 v[16:31], v[130:133], v[168:171], v[16:31]
	v_max3_f32 v126, v126, v94, v95
	v_max3_f32 v126, v126, v64, v65
	v_max3_f32 v126, v126, v66, v67
	v_max3_f32 v126, v126, v68, v69
	v_max3_f32 v126, v126, v70, v71
	v_max3_f32 v126, v126, v72, v73
	v_max3_f32 v126, v126, v74, v75
	v_max3_f32 v126, v126, v76, v77
	v_mfma_f32_32x32x16_bf16 v[16:31], v[134:137], v[172:175], v[16:31]
	v_max3_f32 v126, v126, v78, v79
	v_mov_b32_e32 v127, v126
	s_nop 1
	v_permlane32_swap_b32_e32 v126, v127
	v_max_f32_e32 v127, v127, v127
	v_max_f32_e32 v126, v126, v126
	v_max_f32_e32 v126, v126, v127
	v_sub_f32_e32 v127, v126, v159
	v_cmp_ge_f32_e32 vcc, s19, v127
	v_max_f32_e32 v127, v159, v159
	v_max_f32_e32 v127, v127, v126
	v_mfma_f32_32x32x16_bf16 v[16:31], v[160:163], v[176:179], v[16:31]
	v_sub_f32_e32 v126, v159, v127
	v_mul_f32_e32 v126, 0x3e38aa3b, v126
	v_exp_f32_e32 v126, v126
	s_cmp_eq_u64 vcc, exec
	s_cselect_b64 s[4:5], -1, 0
	v_cndmask_b32_e64 v126, v126, 1.0, s[4:5]
	v_cmp_gt_f32_e32 vcc, 1.0, v126
	s_cbranch_vccz .LBB0_491
	s_and_saveexec_b64 s[0:1], s[2:3]
	ds_write_b32 v145, v126 offset:128
	s_or_b64 exec, exec, s[0:1]
	s_waitcnt lgkmcnt(0)
	v_add_u32_e32 v160, v144, v112
	ds_read_b128 v[128:131], v160 offset:224
	ds_read_b128 v[132:135], v160 offset:192
	ds_read_b128 v[136:139], v160 offset:160
	ds_read_b128 v[160:163], v160 offset:128
	s_waitcnt lgkmcnt(0)
	v_pk_mul_f32 v[12:13], v[12:13], v[128:129]
	v_pk_mul_f32 v[8:9], v[8:9], v[132:133]
	v_pk_mul_f32 v[4:5], v[4:5], v[136:137]
	v_pk_mul_f32 v[14:15], v[14:15], v[130:131]
	v_pk_mul_f32 v[10:11], v[10:11], v[134:135]
	v_pk_mul_f32 v[6:7], v[6:7], v[138:139]
	v_pk_mul_f32 v[2:3], v[2:3], v[162:163]
	v_pk_mul_f32 v[0:1], v[0:1], v[160:161]
	v_pk_mul_f32 v[60:61], v[60:61], v[128:129]
	v_pk_mul_f32 v[56:57], v[56:57], v[132:133]
	v_pk_mul_f32 v[52:53], v[52:53], v[136:137]
	v_pk_mul_f32 v[62:63], v[62:63], v[130:131]
	v_pk_mul_f32 v[58:59], v[58:59], v[134:135]
	v_pk_mul_f32 v[54:55], v[54:55], v[138:139]
	v_pk_mul_f32 v[50:51], v[50:51], v[162:163]
	v_pk_mul_f32 v[48:49], v[48:49], v[160:161]
	v_pk_mul_f32 v[44:45], v[44:45], v[128:129]
	v_pk_mul_f32 v[40:41], v[40:41], v[132:133]
	v_pk_mul_f32 v[36:37], v[36:37], v[136:137]
	v_pk_mul_f32 v[46:47], v[46:47], v[130:131]
	v_pk_mul_f32 v[42:43], v[42:43], v[134:135]
	v_pk_mul_f32 v[38:39], v[38:39], v[138:139]
	v_pk_mul_f32 v[34:35], v[34:35], v[162:163]
	v_pk_mul_f32 v[32:33], v[32:33], v[160:161]
	v_pk_mul_f32 v[28:29], v[28:29], v[128:129]
	v_pk_mul_f32 v[24:25], v[24:25], v[132:133]
	v_pk_mul_f32 v[20:21], v[20:21], v[136:137]
	v_pk_mul_f32 v[30:31], v[30:31], v[130:131]
	v_pk_mul_f32 v[26:27], v[26:27], v[134:135]
	v_pk_mul_f32 v[22:23], v[22:23], v[138:139]
	v_pk_mul_f32 v[18:19], v[18:19], v[162:163]
	v_pk_mul_f32 v[16:17], v[16:17], v[160:161]
.LBB0_491:
	s_add_i32 s0, s18, 4
	s_mul_i32 s1, s0, 0xab
	s_bfe_u32 s1, s1, 0x70009
	s_mul_i32 s1, s1, 3
	s_sub_i32 s0, s0, s1
	s_and_b32 s0, s0, 0xff
	v_cndmask_b32_e64 v127, v127, v159, s[4:5]
	s_lshl_b32 s1, s0, 14
	v_mul_f32_e32 v162, 0xbe38aa3b, v127
	s_add_i32 s1, s14, s1
	s_mulk_i32 s0, 0x6000
	v_fmamk_f32 v184, v64, 0x3e38aa3b, v162
	v_fmamk_f32 v185, v65, 0x3e38aa3b, v162
	s_add_i32 s0, s14, s0
	v_lshl_add_u64 v[64:65], v[118:119], 0, s[24:25]
	s_mov_b32 m0, s1
	s_cmp_eq_u32 s53, 12
	s_cbranch_scc1 .Lilc_w12_da
	s_cmp_eq_u32 s53, 8
	s_cbranch_scc1 .Lilc_w8_da
	s_waitcnt vmcnt(0)
	s_branch .Lilc_wd_da
; #define VM_WAIT() asm volatile("s_waitcnt vmcnt(0)" ::: "memory")
; #define SBAR() __builtin_amdgcn_sched_barrier(0)
; #define RESC(a) do { if (__any((a) < 1.f)) { if (hi == 0) al_l[r32] = (a); asm volatile("s_waitcnt lgkmcnt(0)" ::: "memory"); \
;         _Pragma("unroll") for (int d = 0; d < 4; ++d) _Pragma("unroll") for (int r = 0; r < 16; ++r) o[d][r] *= al_l[crow(r, hi)]; } } while (0)
; template <int MODE>
; __device__ __forceinline__ void partialSM(f32x16& p0, f32x16& p1, float& m_reg, float& mn, float& alpha) {
;     ...
;     const float mnC = -mn * C;
; #pragma unroll
;     for (int r = 0; r < 16; ++r) p0[r] = fmaf(p0[r], C, mnC);
; #pragma unroll
;     for (int r = 0; r < 16; ++r) p1[r] = fmaf(p1[r], C, mnC);
; #pragma unroll
;     for (int r = 0; r < 16; ++r) p0[r] = __builtin_amdgcn_exp2f(p0[r]);
; }
; __device__ __forceinline__ void finishSM(f32x16& p0, f32x16& p1, float alpha, float& l_reg, bf16x8& pa0, bf16x8& pa1, bf16x8& pa2, bf16x8& pa3) {
; #pragma unroll
;     for (int r = 0; r < 16; ++r) p1[r] = __builtin_amdgcn_exp2f(p1[r]);
;     float ps = 0;
; #pragma unroll
;     for (int r = 0; r < 16; ++r) ps += p0[r];
; #pragma unroll
;     for (int r = 0; r < 16; ++r) ps += p1[r];
;     { auto rr = __builtin_amdgcn_permlane32_swap(__float_as_uint(ps), __float_as_uint(ps), false, false);
;       ps = __uint_as_float(rr[0]) + __uint_as_float(rr[1]); }
;     l_reg = l_reg * alpha + ps;
;     ...
;     PK4(p0, 0, pa0); PK4(p0, 8, pa1); PK4(p1, 0, pa2); PK4(p1, 8, pa3);
;     ...
; }
;     ...
;             RESC(alB); VM_WAIT(); __syncthreads();
;             if (j + 2 < NT) GLDS3(j + 2);
;             SBAR(); qkt<MODE>(p0, p1, KB3(j + 1), qr, r32, hi);
;             finishSM(pB0, pB1, alB, l_reg, pa0, pa1, pa2, pa3); SBAR();
;             pv_d0(o, VB3(j), pa0, pa1, pa2, pa3); partialSM<MODE>(p0, p1, m_reg, mn, al);
.Lilc_w12_da:
	s_waitcnt vmcnt(12)
	s_branch .Lilc_wd_da
.Lilc_w8_da:
	s_waitcnt vmcnt(8)
.Lilc_wd_da:
	s_barrier
	s_add_i32 s4, s0, 0xc000
	global_load_lds_dwordx4 v[64:65], off
	v_lshl_add_u64 v[64:65], v[120:121], 0, s[24:25]
	s_add_i32 m0, s1, 0x2000
	s_mov_b64 s[0:1], 0x2981880
	global_load_lds_dwordx4 v[64:65], off
	v_lshl_add_u64 v[64:65], v[122:123], 0, s[0:1]
	s_mov_b32 m0, s4
	v_fmamk_f32 v80, v80, 0x3e38aa3b, v162
	global_load_lds_dwordx4 v[64:65], off
	v_fmamk_f32 v81, v81, 0x3e38aa3b, v162
	v_fmamk_f32 v82, v82, 0x3e38aa3b, v162
	v_fmamk_f32 v83, v83, 0x3e38aa3b, v162
	v_fmamk_f32 v84, v84, 0x3e38aa3b, v162
	v_fmamk_f32 v85, v85, 0x3e38aa3b, v162
	v_fmamk_f32 v86, v86, 0x3e38aa3b, v162
	v_fmamk_f32 v87, v87, 0x3e38aa3b, v162
	v_fmamk_f32 v88, v88, 0x3e38aa3b, v162
	v_fmamk_f32 v89, v89, 0x3e38aa3b, v162
	v_fmamk_f32 v90, v90, 0x3e38aa3b, v162
	v_fmamk_f32 v91, v91, 0x3e38aa3b, v162
	v_fmamk_f32 v92, v92, 0x3e38aa3b, v162
	v_fmamk_f32 v93, v93, 0x3e38aa3b, v162
	v_fmamk_f32 v94, v94, 0x3e38aa3b, v162
	v_fmamk_f32 v95, v95, 0x3e38aa3b, v162
	v_fmamk_f32 v186, v66, 0x3e38aa3b, v162
	v_fmamk_f32 v187, v67, 0x3e38aa3b, v162
	v_fmamk_f32 v188, v68, 0x3e38aa3b, v162
	v_fmamk_f32 v189, v69, 0x3e38aa3b, v162
	v_fmamk_f32 v190, v70, 0x3e38aa3b, v162
	v_fmamk_f32 v191, v71, 0x3e38aa3b, v162
	v_fmamk_f32 v194, v72, 0x3e38aa3b, v162
	v_fmamk_f32 v195, v73, 0x3e38aa3b, v162
	v_fmamk_f32 v196, v74, 0x3e38aa3b, v162
	v_fmamk_f32 v197, v75, 0x3e38aa3b, v162
	v_fmamk_f32 v198, v76, 0x3e38aa3b, v162
	v_fmamk_f32 v199, v77, 0x3e38aa3b, v162
	v_fmamk_f32 v200, v78, 0x3e38aa3b, v162
	v_fmac_f32_e32 v162, 0x3e38aa3b, v79
	v_exp_f32_e32 v136, v80
	v_exp_f32_e32 v137, v81
	v_exp_f32_e32 v138, v82
	v_exp_f32_e32 v139, v83
	v_exp_f32_e32 v159, v84
	v_exp_f32_e32 v160, v85
	v_exp_f32_e32 v161, v86
	v_exp_f32_e32 v163, v87
	v_exp_f32_e32 v128, v88
	v_exp_f32_e32 v129, v89
	v_exp_f32_e32 v130, v90
	v_exp_f32_e32 v131, v91
	v_exp_f32_e32 v132, v92
	v_exp_f32_e32 v133, v93
	v_exp_f32_e32 v134, v94
	v_exp_f32_e32 v135, v95
	v_add_u32_e32 v72, s17, v148
	v_add_u32_e32 v68, v72, v150
	v_add_u32_e32 v73, v72, v154
	ds_read_b128 v[64:67], v68 offset:49152
	ds_read_b128 v[68:71], v68 offset:53248
	ds_read_b128 v[118:121], v73 offset:49152
	ds_read_b128 v[164:167], v73 offset:53248
	v_add_u32_e32 v73, v72, v155
	ds_read_b128 v[168:171], v73 offset:49152
	ds_read_b128 v[172:175], v73 offset:53248
	s_waitcnt lgkmcnt(0)
	v_mfma_f32_32x32x16_bf16 v[80:95], v[64:67], v[104:107], 0
	v_add_u32_e32 v64, v72, v157
	ds_read_b128 v[176:179], v64 offset:49152
	ds_read_b128 v[180:183], v64 offset:53248
	v_mfma_f32_32x32x16_bf16 v[64:79], v[68:71], v[104:107], 0
	v_mfma_f32_32x32x16_bf16 v[80:95], v[118:121], v[108:111], v[80:95]
	v_mfma_f32_32x32x16_bf16 v[64:79], v[164:167], v[108:111], v[64:79]
	v_mfma_f32_32x32x16_bf16 v[80:95], v[168:171], v[100:103], v[80:95]
	v_mfma_f32_32x32x16_bf16 v[64:79], v[172:175], v[100:103], v[64:79]
	s_waitcnt lgkmcnt(0)
	v_mfma_f32_32x32x16_bf16 v[80:95], v[176:179], v[96:99], v[80:95]
	v_mfma_f32_32x32x16_bf16 v[64:79], v[180:183], v[96:99], v[64:79]
	v_add_f32_e32 v120, 0, v136
	v_add_f32_e32 v120, v137, v120
	v_add_f32_e32 v120, v138, v120
	v_add_f32_e32 v120, v139, v120
	v_add_f32_e32 v120, v159, v120
	v_add_f32_e32 v120, v160, v120
	v_add_f32_e32 v120, v161, v120
	v_add_f32_e32 v120, v163, v120
	v_add_f32_e32 v120, v128, v120
	v_add_f32_e32 v120, v129, v120
	v_add_f32_e32 v120, v130, v120
	v_add_f32_e32 v120, v131, v120
	v_exp_f32_e32 v118, v184
	v_add_f32_e32 v120, v132, v120
	v_exp_f32_e32 v119, v185
	v_add_f32_e32 v120, v133, v120
	v_exp_f32_e32 v122, v186
	v_add_f32_e32 v120, v134, v120
	v_exp_f32_e32 v123, v187
	v_add_f32_e32 v120, v135, v120
	v_exp_f32_e32 v164, v188
	v_add_f32_e32 v120, v118, v120
	v_exp_f32_e32 v165, v189
	v_add_f32_e32 v120, v119, v120
	v_exp_f32_e32 v166, v190
	v_add_f32_e32 v120, v122, v120
	v_exp_f32_e32 v167, v191
	v_add_f32_e32 v120, v123, v120
	v_exp_f32_e32 v168, v194
	v_add_f32_e32 v120, v164, v120
	v_exp_f32_e32 v169, v195
	v_add_f32_e32 v120, v165, v120
	v_exp_f32_e32 v170, v196
	v_add_f32_e32 v120, v166, v120
	v_exp_f32_e32 v171, v197
	v_add_f32_e32 v120, v167, v120
	v_exp_f32_e32 v172, v198
	v_add_f32_e32 v120, v168, v120
	v_exp_f32_e32 v173, v199
	v_add_f32_e32 v120, v169, v120
	v_exp_f32_e32 v174, v200
	v_add_f32_e32 v120, v170, v120
	v_exp_f32_e32 v175, v162
	v_add_f32_e32 v120, v171, v120
	v_add_f32_e32 v120, v172, v120
	v_add_f32_e32 v120, v173, v120
	v_add_f32_e32 v120, v174, v120
	v_add_f32_e32 v120, v175, v120
	v_mov_b32_e32 v121, v120
	s_nop 1
	v_permlane32_swap_b32_e32 v120, v121
	v_cvt_pk_bf16_f32 v136, v136, v137
	v_cvt_pk_bf16_f32 v137, v138, v139
	v_cvt_pk_bf16_f32 v138, v159, v160
	v_cvt_pk_bf16_f32 v139, v161, v163
	v_cvt_pk_bf16_f32 v128, v128, v129
	v_cvt_pk_bf16_f32 v129, v130, v131
	v_cvt_pk_bf16_f32 v130, v132, v133
	v_cvt_pk_bf16_f32 v131, v134, v135
	v_cvt_pk_bf16_f32 v132, v118, v119
	v_cvt_pk_bf16_f32 v133, v122, v123
	v_cvt_pk_bf16_f32 v134, v164, v165
	v_cvt_pk_bf16_f32 v135, v166, v167
	v_cvt_pk_bf16_f32 v160, v168, v169
	v_cvt_pk_bf16_f32 v161, v170, v171
	v_cvt_pk_bf16_f32 v162, v172, v173
	v_cvt_pk_bf16_f32 v163, v174, v175
	s_nop 0
	v_permlane32_swap_b32_e32 v136, v138
	v_permlane32_swap_b32_e32 v137, v139
	v_permlane32_swap_b32_e32 v128, v130
	v_permlane32_swap_b32_e32 v129, v131
	v_permlane32_swap_b32_e32 v132, v134
	v_permlane32_swap_b32_e32 v133, v135
	v_permlane32_swap_b32_e32 v160, v162
	v_permlane32_swap_b32_e32 v161, v163
	v_lshl_add_u32 v118, s16, 14, v113
	ds_read_b64_tr_b16 v[164:165], v118 offset:0
	ds_read_b64_tr_b16 v[166:167], v118 offset:0x800
	ds_read_b64_tr_b16 v[168:169], v118 offset:0x1000
	ds_read_b64_tr_b16 v[170:171], v118 offset:0x1800
	ds_read_b64_tr_b16 v[172:173], v118 offset:0x2000
	ds_read_b64_tr_b16 v[174:175], v118 offset:0x2800
	ds_read_b64_tr_b16 v[176:177], v118 offset:0x3000
	ds_read_b64_tr_b16 v[178:179], v118 offset:0x3800
	s_waitcnt lgkmcnt(0)
; #define VM_WAIT() asm volatile("s_waitcnt vmcnt(0)" ::: "memory")
; #define SBAR() __builtin_amdgcn_sched_barrier(0)
; #define RESC(a) do { if (__any((a) < 1.f)) { if (hi == 0) al_l[r32] = (a); asm volatile("s_waitcnt lgkmcnt(0)" ::: "memory"); \
;         _Pragma("unroll") for (int d = 0; d < 4; ++d) _Pragma("unroll") for (int r = 0; r < 16; ++r) o[d][r] *= al_l[crow(r, hi)]; } } while (0)
; template <int D0> __device__ __forceinline__ void pv_one(f32x16& od, int vb, bf16x8 pa0, bf16x8 pa1, bf16x8 pa2, bf16x8 pa3) {
;     const s16x4 l0 = tr_read<v_rd_off(D0, 0, 0)>(vb), h0 = tr_read<v_rd_off(D0, 0, 1)>(vb), l1 = tr_read<v_rd_off(D0, 1, 0)>(vb), h1 = tr_read<v_rd_off(D0, 1, 1)>(vb);
;     const s16x4 l2 = tr_read<v_rd_off(D0, 2, 0)>(vb), h2 = tr_read<v_rd_off(D0, 2, 1)>(vb), l3 = tr_read<v_rd_off(D0, 3, 0)>(vb), h3 = tr_read<v_rd_off(D0, 3, 1)>(vb);
;     asm volatile("s_waitcnt lgkmcnt(0)" ::: "memory"); SBAR();
;     ...
;     od = __builtin_amdgcn_mfma_f32_32x32x16_bf16(pa0, PK(l0, h0), od, 0, 0, 0);
;     od = __builtin_amdgcn_mfma_f32_32x32x16_bf16(pa1, PK(l1, h1), od, 0, 0, 0);
;     od = __builtin_amdgcn_mfma_f32_32x32x16_bf16(pa2, PK(l2, h2), od, 0, 0, 0);
;     od = __builtin_amdgcn_mfma_f32_32x32x16_bf16(pa3, PK(l3, h3), od, 0, 0, 0);
;     ...
; }
; __device__ __forceinline__ void pv_d0(f32x16* o, int vb, bf16x8 pa0, bf16x8 pa1, bf16x8 pa2, bf16x8 pa3) {
;     pv_one<0>(o[0], vb, pa0, pa1, pa2, pa3); pv_one<1>(o[1], vb, pa0, pa1, pa2, pa3); pv_one<2>(o[2], vb, pa0, pa1, pa2, pa3); pv_one<3>(o[3], vb, pa0, pa1, pa2, pa3);
; }
;     ...
;             pv_d0(o, VB3(j), pa0, pa1, pa2, pa3); partialSM<MODE>(p0, p1, m_reg, mn, al);
;             RESC(al); VM_WAIT(); __syncthreads();
	s_nop 0
	v_mfma_f32_32x32x16_bf16 v[0:15], v[136:139], v[164:167], v[0:15]
	ds_read_b64_tr_b16 v[164:165], v118 offset:0x200
	ds_read_b64_tr_b16 v[166:167], v118 offset:0xa00
	v_mfma_f32_32x32x16_bf16 v[0:15], v[128:131], v[168:171], v[0:15]
	ds_read_b64_tr_b16 v[168:169], v118 offset:0x1200
	ds_read_b64_tr_b16 v[170:171], v118 offset:0x1a00
	v_mfma_f32_32x32x16_bf16 v[0:15], v[132:135], v[172:175], v[0:15]
	ds_read_b64_tr_b16 v[172:173], v118 offset:0x2200
	ds_read_b64_tr_b16 v[174:175], v118 offset:0x2a00
	v_mfma_f32_32x32x16_bf16 v[0:15], v[160:163], v[176:179], v[0:15]
	ds_read_b64_tr_b16 v[176:177], v118 offset:0x3200
	ds_read_b64_tr_b16 v[178:179], v118 offset:0x3a00
	s_waitcnt lgkmcnt(0)
	v_mfma_f32_32x32x16_bf16 v[48:63], v[136:139], v[164:167], v[48:63]
	ds_read_b64_tr_b16 v[164:165], v118 offset:0x400
	ds_read_b64_tr_b16 v[166:167], v118 offset:0xc00
	v_mfma_f32_32x32x16_bf16 v[48:63], v[128:131], v[168:171], v[48:63]
	ds_read_b64_tr_b16 v[168:169], v118 offset:0x1400
	ds_read_b64_tr_b16 v[170:171], v118 offset:0x1c00
	v_mfma_f32_32x32x16_bf16 v[48:63], v[132:135], v[172:175], v[48:63]
	ds_read_b64_tr_b16 v[172:173], v118 offset:0x2400
	ds_read_b64_tr_b16 v[174:175], v118 offset:0x2c00
	v_mfma_f32_32x32x16_bf16 v[48:63], v[160:163], v[176:179], v[48:63]
	ds_read_b64_tr_b16 v[176:177], v118 offset:0x3400
	ds_read_b64_tr_b16 v[178:179], v118 offset:0x3c00
	s_waitcnt lgkmcnt(0)
	v_mfma_f32_32x32x16_bf16 v[32:47], v[136:139], v[164:167], v[32:47]
	ds_read_b64_tr_b16 v[164:165], v118 offset:0x600
	ds_read_b64_tr_b16 v[166:167], v118 offset:0xe00
	v_mfma_f32_32x32x16_bf16 v[32:47], v[128:131], v[168:171], v[32:47]
	ds_read_b64_tr_b16 v[168:169], v118 offset:0x1600
	ds_read_b64_tr_b16 v[170:171], v118 offset:0x1e00
	v_mfma_f32_32x32x16_bf16 v[32:47], v[132:135], v[172:175], v[32:47]
	ds_read_b64_tr_b16 v[172:173], v118 offset:0x2600
	ds_read_b64_tr_b16 v[174:175], v118 offset:0x2e00
	v_mfma_f32_32x32x16_bf16 v[32:47], v[160:163], v[176:179], v[32:47]
	ds_read_b64_tr_b16 v[176:177], v118 offset:0x3600
	ds_read_b64_tr_b16 v[178:179], v118 offset:0x3e00
	s_waitcnt lgkmcnt(0)
	v_mfma_f32_32x32x16_bf16 v[16:31], v[136:139], v[164:167], v[16:31]
	v_max_f32_e32 v118, v81, v81
	v_max_f32_e32 v119, v80, v80
	v_max_f32_e32 v118, v119, v118
	v_max3_f32 v118, v118, v82, v83
	v_max3_f32 v118, v118, v84, v85
	v_max3_f32 v118, v118, v86, v87
	v_max3_f32 v118, v118, v88, v89
	v_max3_f32 v118, v118, v90, v91
	v_max3_f32 v118, v118, v92, v93
	v_mfma_f32_32x32x16_bf16 v[16:31], v[128:131], v[168:171], v[16:31]
	v_max3_f32 v118, v118, v94, v95
	v_max3_f32 v118, v118, v64, v65
	v_max3_f32 v118, v118, v66, v67
	v_max3_f32 v118, v118, v68, v69
	v_max3_f32 v118, v118, v70, v71
	v_max3_f32 v118, v118, v72, v73
	v_max3_f32 v118, v118, v74, v75
	v_max3_f32 v118, v118, v76, v77
	v_mfma_f32_32x32x16_bf16 v[16:31], v[132:135], v[172:175], v[16:31]
	v_max3_f32 v118, v118, v78, v79
	v_mov_b32_e32 v119, v118
	s_nop 1
	v_permlane32_swap_b32_e32 v118, v119
	v_max_f32_e32 v119, v119, v119
	v_max_f32_e32 v118, v118, v118
	v_max_f32_e32 v118, v118, v119
	v_sub_f32_e32 v119, v118, v127
	v_cmp_ge_f32_e32 vcc, s19, v119
	v_max_f32_e32 v119, v127, v127
	v_max_f32_e32 v118, v119, v118
	v_mfma_f32_32x32x16_bf16 v[16:31], v[160:163], v[176:179], v[16:31]
	v_sub_f32_e32 v119, v127, v118
	v_mul_f32_e32 v119, 0x3e38aa3b, v119
	v_exp_f32_e32 v119, v119
	s_cmp_eq_u64 vcc, exec
	s_cselect_b64 s[4:5], -1, 0
	v_cndmask_b32_e64 v119, v119, 1.0, s[4:5]
	v_cmp_gt_f32_e32 vcc, 1.0, v119
	s_cbranch_vccz .LBB0_495
	s_and_saveexec_b64 s[0:1], s[2:3]
	ds_write_b32 v145, v119 offset:128
	s_or_b64 exec, exec, s[0:1]
	s_waitcnt lgkmcnt(0)
	v_add_u32_e32 v122, v144, v112
	ds_read_b128 v[128:131], v122 offset:224
	ds_read_b128 v[132:135], v122 offset:192
	ds_read_b128 v[136:139], v122 offset:160
	ds_read_b128 v[160:163], v122 offset:128
	s_waitcnt lgkmcnt(0)
	v_pk_mul_f32 v[12:13], v[12:13], v[128:129]
	v_pk_mul_f32 v[8:9], v[8:9], v[132:133]
	v_pk_mul_f32 v[4:5], v[4:5], v[136:137]
	v_pk_mul_f32 v[14:15], v[14:15], v[130:131]
	v_pk_mul_f32 v[10:11], v[10:11], v[134:135]
	v_pk_mul_f32 v[6:7], v[6:7], v[138:139]
	v_pk_mul_f32 v[2:3], v[2:3], v[162:163]
	v_pk_mul_f32 v[0:1], v[0:1], v[160:161]
	v_pk_mul_f32 v[60:61], v[60:61], v[128:129]
	v_pk_mul_f32 v[56:57], v[56:57], v[132:133]
	v_pk_mul_f32 v[52:53], v[52:53], v[136:137]
	v_pk_mul_f32 v[62:63], v[62:63], v[130:131]
	v_pk_mul_f32 v[58:59], v[58:59], v[134:135]
	v_pk_mul_f32 v[54:55], v[54:55], v[138:139]
	v_pk_mul_f32 v[50:51], v[50:51], v[162:163]
	v_pk_mul_f32 v[48:49], v[48:49], v[160:161]
	v_pk_mul_f32 v[44:45], v[44:45], v[128:129]
	v_pk_mul_f32 v[40:41], v[40:41], v[132:133]
	v_pk_mul_f32 v[36:37], v[36:37], v[136:137]
	v_pk_mul_f32 v[46:47], v[46:47], v[130:131]
	v_pk_mul_f32 v[42:43], v[42:43], v[134:135]
	v_pk_mul_f32 v[38:39], v[38:39], v[138:139]
	v_pk_mul_f32 v[34:35], v[34:35], v[162:163]
	v_pk_mul_f32 v[32:33], v[32:33], v[160:161]
	v_pk_mul_f32 v[28:29], v[28:29], v[128:129]
	v_pk_mul_f32 v[24:25], v[24:25], v[132:133]
	v_pk_mul_f32 v[20:21], v[20:21], v[136:137]
	v_pk_mul_f32 v[30:31], v[30:31], v[130:131]
	v_pk_mul_f32 v[26:27], v[26:27], v[134:135]
	v_pk_mul_f32 v[22:23], v[22:23], v[138:139]
	v_pk_mul_f32 v[18:19], v[18:19], v[162:163]
	v_pk_mul_f32 v[16:17], v[16:17], v[160:161]

; #define VM_WAIT() asm volatile("s_waitcnt vmcnt(0)" ::: "memory")
;     __device__ __forceinline__ const float* in(int i) const { return *(const float* const __attribute__((address_space(4)))*)(p + 8 * i); }
;     __device__ __forceinline__ unsigned char* ws() const { return *(unsigned char* const __attribute__((address_space(4)))*)(p + 232); }
;     ...
;         f32x16 pB0, pB1; float mnB, alB;
;         GLDS3(0); GLDS3(1); VM_WAIT(); __syncthreads();
;         qkt<MODE>(p0, p1, KB3(0), qr, r32, hi); partialSM<MODE>(p0, p1, m_reg, mn, al);
; #pragma unroll 1
;         for (int j = 1; j + 1 < NT; j += 2) {
;             GLDS3(j + 1);
; __device__ __forceinline__ CvtDesc conv_expert_desc(const KA& a, unsigned char* ws, int q) {
;     const int l = q / Q_PER_L; int r = q - l * Q_PER_L;
;     unsigned char* wl = ws + WS_W + (size_t)l * W_LSTRIDE;
;     CvtDesc d; d.f8 = (MOE_FP8_LAST && (MOE_FP8_GU_ALL || l == NLAYER - 1)) ? 1 : 0;
;     if (MOE_FP8_LAST && MOE_FP8_DOWN_ALL && r >= 2 * Q_IG) d.f8 = 1;
;     const int eb = d.f8 ? 1 : 2;
;     if (r < 2 * Q_IG) { const int up = r >= Q_IG; if (up) r -= Q_IG; const int e = r >> 8, rr = r & 255, kb = rr >> 3, nb = rr & 7, n0 = nb * 64;
;         const float* src = e < 64 ? a.in(up ? 21 : 20) + ((size_t)l * 64 + e) * DM * FFE : a.in(up ? 24 : 23) + (size_t)l * DM * FFE;
.LBB0_499:
	s_mul_i32 s0, s16, 0xab
	s_addk_i32 s0, 0x201
	s_bfe_u32 s0, s0, 0x70009
	s_mul_i32 s0, s0, 3
	s_sub_i32 s0, s16, s0
	s_add_i32 s0, s0, 3
	s_and_b32 s0, s0, 0xff
	s_lshl_b32 s1, s0, 14
	s_mulk_i32 s0, 0x6000
	s_add_i32 s1, s12, s1
	s_add_i32 s15, s0, 0
	v_lshl_add_u64 v[118:119], s[6:7], 0, v[114:115]
	s_add_i32 s0, s15, s11
	v_lshl_add_u64 v[64:65], v[118:119], 0, s[20:21]
	s_mov_b32 m0, s1
	v_lshl_add_u64 v[120:121], s[6:7], 0, v[116:117]
	s_add_i32 s4, s0, 0xc000
	global_load_lds_dwordx4 v[64:65], off
	v_lshl_add_u64 v[64:65], v[120:121], 0, s[20:21]
	s_add_i32 m0, s1, 0x2000
	v_lshl_add_u64 v[122:123], s[6:7], 0, v[192:193]
	s_mov_b64 s[0:1], 0x2901800
	global_load_lds_dwordx4 v[64:65], off
	v_lshl_add_u64 v[64:65], v[122:123], 0, s[0:1]
	s_mov_b32 m0, s4
	s_add_i32 s13, s16, 2
	global_load_lds_dwordx4 v[64:65], off
	s_add_u32 s52, s52, 16
	s_cmp_ge_u32 s52, 31
	s_cselect_b32 s50, 1, 0
	s_cbranch_scc0 .Lilc_n_db
	s_sub_u32 s52, s52, 31
	s_mov_b32 s46, s51
	s_add_u32 s51, s51, 1
	s_lshl_b32 s49, s46, 2
	s_add_u32 s49, s49, s54
	s_cmp_lt_u32 s49, 0xc3
	s_cselect_b32 s50, 1, 0
	s_cbranch_scc0 .Lilc_n_db
	s_lshr_b32 s55, s46, 4
	s_and_b32 s57, s49, 63
	s_lshl_b32 s101, s56, 6
	s_add_u32 s101, s101, s57
	s_cmp_eq_u32 s55, 3
	s_cselect_b32 s55, s54, s55
	s_cselect_b32 s100, 3, 0
	s_cselect_b32 s101, s56, s101
	s_cselect_b32 s57, 64, s57
	s_add_u32 s100, s100, s55
	s_lshl_b32 s100, s100, 3
	s_add_u32 s100, s100, 0xa0
	s_load_dwordx2 s[44:45], s[36:37], s100

; #define SBAR() __builtin_amdgcn_sched_barrier(0)
; __device__ __forceinline__ void finishSM(f32x16& p0, f32x16& p1, float alpha, float& l_reg, bf16x8& pa0, bf16x8& pa1, bf16x8& pa2, bf16x8& pa3) {
; #pragma unroll
;     for (int r = 0; r < 16; ++r) p1[r] = __builtin_amdgcn_exp2f(p1[r]);
;     float ps = 0;
; #pragma unroll
;     for (int r = 0; r < 16; ++r) ps += p0[r];
; #pragma unroll
;     for (int r = 0; r < 16; ++r) ps += p1[r];
;     { auto rr = __builtin_amdgcn_permlane32_swap(__float_as_uint(ps), __float_as_uint(ps), false, false);
;       ps = __uint_as_float(rr[0]) + __uint_as_float(rr[1]); }
;     l_reg = l_reg * alpha + ps;
;     ...
;     PK4(p0, 0, pa0); PK4(p0, 8, pa1); PK4(p1, 0, pa2); PK4(p1, 8, pa3);
;     ...
; }
;     ...
;             SBAR(); qkt<MODE>(pB0, pB1, KB3(j), qr, r32, hi);
;             finishSM(p0, p1, al, l_reg, pa0, pa1, pa2, pa3); SBAR();
;             pv_d0(o, VB3(j - 1), pa0, pa1, pa2, pa3); partialSM<MODE>(pB0, pB1, m_reg, mnB, alB);
.Lilc_d_db:
	s_mul_i32 s0, s13, 0xab
	s_bfe_u32 s0, s0, 0x70009
	s_mul_i32 s0, s0, 3
	s_sub_i32 s0, s13, s0
	s_and_b32 s14, s0, 0xff
	s_mul_i32 s0, s14, 0x6000
	v_add_u32_e32 v72, s0, v151
	v_add_u32_e32 v68, v72, v149
	v_add_u32_e32 v73, v72, v153
	ds_read_b128 v[64:67], v68 offset:49152
	ds_read_b128 v[68:71], v68 offset:53248
	ds_read_b128 v[176:179], v73 offset:49152
	ds_read_b128 v[180:183], v73 offset:53248
	v_add_u32_e32 v73, v72, v154
	ds_read_b128 v[184:187], v73 offset:49152
	ds_read_b128 v[188:191], v73 offset:53248
	s_waitcnt lgkmcnt(0)
	v_mfma_f32_32x32x16_bf16 v[80:95], v[64:67], v[104:107], 0
	v_add_u32_e32 v64, v72, v156
	ds_read_b128 v[194:197], v64 offset:49152
	ds_read_b128 v[198:201], v64 offset:53248
	v_mfma_f32_32x32x16_bf16 v[64:79], v[68:71], v[104:107], 0
	v_mfma_f32_32x32x16_bf16 v[80:95], v[176:179], v[108:111], v[80:95]
	v_mfma_f32_32x32x16_bf16 v[64:79], v[180:183], v[108:111], v[64:79]
	v_mfma_f32_32x32x16_bf16 v[80:95], v[184:187], v[100:103], v[80:95]
	v_mfma_f32_32x32x16_bf16 v[64:79], v[188:191], v[100:103], v[64:79]
	s_waitcnt lgkmcnt(0)
	v_mfma_f32_32x32x16_bf16 v[80:95], v[194:197], v[96:99], v[80:95]
	v_mfma_f32_32x32x16_bf16 v[64:79], v[198:201], v[96:99], v[64:79]
	v_exp_f32_e32 v185, v124
	v_add_f32_e32 v124, 0, v172
	v_add_f32_e32 v124, v174, v124
	v_add_f32_e32 v124, v170, v124
	v_add_f32_e32 v124, v173, v124
	v_add_f32_e32 v124, v168, v124
	v_add_f32_e32 v124, v171, v124
	v_add_f32_e32 v124, v167, v124
	v_add_f32_e32 v124, v169, v124
	v_add_f32_e32 v124, v164, v124
	v_add_f32_e32 v124, v166, v124
	v_add_f32_e32 v124, v162, v124
	v_add_f32_e32 v124, v165, v124
	v_exp_f32_e32 v138, v138
	v_add_f32_e32 v124, v160, v124
	v_exp_f32_e32 v139, v139
	v_add_f32_e32 v124, v163, v124
	v_exp_f32_e32 v136, v136
	v_add_f32_e32 v124, v159, v124
	v_exp_f32_e32 v137, v137
	v_add_f32_e32 v124, v161, v124
	v_exp_f32_e32 v175, v134
	v_add_f32_e32 v124, v138, v124
	v_exp_f32_e32 v176, v135
	v_add_f32_e32 v124, v139, v124
	v_exp_f32_e32 v177, v132
	v_add_f32_e32 v124, v136, v124
	v_exp_f32_e32 v178, v133
	v_add_f32_e32 v124, v137, v124
	v_exp_f32_e32 v179, v130
	v_add_f32_e32 v124, v175, v124
	v_exp_f32_e32 v180, v131
	v_add_f32_e32 v124, v176, v124
	v_exp_f32_e32 v181, v128
	v_add_f32_e32 v124, v177, v124
	v_exp_f32_e32 v182, v129
	v_add_f32_e32 v124, v178, v124
	v_exp_f32_e32 v183, v126
	v_add_f32_e32 v124, v179, v124
	v_exp_f32_e32 v184, v127
	v_add_f32_e32 v124, v180, v124
	v_add_f32_e32 v124, v181, v124
	v_exp_f32_e32 v186, v125
	v_add_f32_e32 v124, v182, v124
	v_add_f32_e32 v124, v183, v124
	v_add_f32_e32 v124, v184, v124
	v_add_f32_e32 v124, v185, v124
	v_add_f32_e32 v124, v186, v124
	v_mov_b32_e32 v125, v124
	v_cvt_pk_bf16_f32 v126, v172, v174
	v_cvt_pk_bf16_f32 v127, v170, v173
	v_cvt_pk_bf16_f32 v128, v168, v171
	v_cvt_pk_bf16_f32 v129, v167, v169
	s_nop 1
	v_permlane32_swap_b32_e32 v124, v125
	v_permlane32_swap_b32_e32 v126, v128
	v_permlane32_swap_b32_e32 v127, v129
	v_cvt_pk_bf16_f32 v130, v164, v166
	v_cvt_pk_bf16_f32 v131, v162, v165
	v_cvt_pk_bf16_f32 v132, v160, v163
	v_cvt_pk_bf16_f32 v133, v159, v161
	v_cvt_pk_bf16_f32 v134, v138, v139
	v_cvt_pk_bf16_f32 v135, v136, v137
	v_cvt_pk_bf16_f32 v136, v175, v176
	v_cvt_pk_bf16_f32 v137, v177, v178
	v_cvt_pk_bf16_f32 v160, v179, v180
	v_cvt_pk_bf16_f32 v161, v181, v182
	v_cvt_pk_bf16_f32 v162, v183, v184
	v_cvt_pk_bf16_f32 v163, v185, v186
	s_nop 0
	v_permlane32_swap_b32_e32 v130, v132
	v_permlane32_swap_b32_e32 v131, v133
	v_permlane32_swap_b32_e32 v134, v136
	v_permlane32_swap_b32_e32 v135, v137
	v_permlane32_swap_b32_e32 v160, v162
	v_permlane32_swap_b32_e32 v161, v163
	s_add_i32 s0, s16, 0x10001
	s_and_b32 s1, s0, 0xff
	s_mulk_i32 s1, 0xab
	s_bfe_u32 s1, s1, 0x70009
	s_mul_i32 s1, s1, 3
	s_sub_i32 s0, s0, s1
	s_and_b32 s0, s0, 0xff
	v_lshl_add_u32 v138, s0, 14, v113
	ds_read_b64_tr_b16 v[164:165], v138 offset:0
	ds_read_b64_tr_b16 v[166:167], v138 offset:0x800
	ds_read_b64_tr_b16 v[168:169], v138 offset:0x1000
	ds_read_b64_tr_b16 v[170:171], v138 offset:0x1800
	ds_read_b64_tr_b16 v[172:173], v138 offset:0x2000
	ds_read_b64_tr_b16 v[174:175], v138 offset:0x2800
	ds_read_b64_tr_b16 v[176:177], v138 offset:0x3000
	ds_read_b64_tr_b16 v[178:179], v138 offset:0x3800
	s_waitcnt lgkmcnt(0)
	s_nop 0
	v_mfma_f32_32x32x16_bf16 v[0:15], v[126:129], v[164:167], v[0:15]
	ds_read_b64_tr_b16 v[164:165], v138 offset:0x200
	ds_read_b64_tr_b16 v[166:167], v138 offset:0xa00
	v_mfma_f32_32x32x16_bf16 v[0:15], v[130:133], v[168:171], v[0:15]
	ds_read_b64_tr_b16 v[168:169], v138 offset:0x1200
	ds_read_b64_tr_b16 v[170:171], v138 offset:0x1a00
	v_mfma_f32_32x32x16_bf16 v[0:15], v[134:137], v[172:175], v[0:15]
	ds_read_b64_tr_b16 v[172:173], v138 offset:0x2200
	ds_read_b64_tr_b16 v[174:175], v138 offset:0x2a00
	v_mfma_f32_32x32x16_bf16 v[0:15], v[160:163], v[176:179], v[0:15]
	ds_read_b64_tr_b16 v[176:177], v138 offset:0x3200
	ds_read_b64_tr_b16 v[178:179], v138 offset:0x3a00
	s_waitcnt lgkmcnt(0)
; #define VM_WAIT() asm volatile("s_waitcnt vmcnt(0)" ::: "memory")
; #define SBAR() __builtin_amdgcn_sched_barrier(0)
; #define RESC(a) do { if (__any((a) < 1.f)) { if (hi == 0) al_l[r32] = (a); asm volatile("s_waitcnt lgkmcnt(0)" ::: "memory"); \
;         _Pragma("unroll") for (int d = 0; d < 4; ++d) _Pragma("unroll") for (int r = 0; r < 16; ++r) o[d][r] *= al_l[crow(r, hi)]; } } while (0)
; template <int D0> __device__ __forceinline__ void pv_one(f32x16& od, int vb, bf16x8 pa0, bf16x8 pa1, bf16x8 pa2, bf16x8 pa3) {
;     const s16x4 l0 = tr_read<v_rd_off(D0, 0, 0)>(vb), h0 = tr_read<v_rd_off(D0, 0, 1)>(vb), l1 = tr_read<v_rd_off(D0, 1, 0)>(vb), h1 = tr_read<v_rd_off(D0, 1, 1)>(vb);
;     const s16x4 l2 = tr_read<v_rd_off(D0, 2, 0)>(vb), h2 = tr_read<v_rd_off(D0, 2, 1)>(vb), l3 = tr_read<v_rd_off(D0, 3, 0)>(vb), h3 = tr_read<v_rd_off(D0, 3, 1)>(vb);
;     asm volatile("s_waitcnt lgkmcnt(0)" ::: "memory"); SBAR();
;     ...
;     od = __builtin_amdgcn_mfma_f32_32x32x16_bf16(pa0, PK(l0, h0), od, 0, 0, 0);
;     od = __builtin_amdgcn_mfma_f32_32x32x16_bf16(pa1, PK(l1, h1), od, 0, 0, 0);
;     od = __builtin_amdgcn_mfma_f32_32x32x16_bf16(pa2, PK(l2, h2), od, 0, 0, 0);
;     od = __builtin_amdgcn_mfma_f32_32x32x16_bf16(pa3, PK(l3, h3), od, 0, 0, 0);
;     ...
; }
; __device__ __forceinline__ void pv_d0(f32x16* o, int vb, bf16x8 pa0, bf16x8 pa1, bf16x8 pa2, bf16x8 pa3) {
;     pv_one<0>(o[0], vb, pa0, pa1, pa2, pa3); pv_one<1>(o[1], vb, pa0, pa1, pa2, pa3); pv_one<2>(o[2], vb, pa0, pa1, pa2, pa3); pv_one<3>(o[3], vb, pa0, pa1, pa2, pa3);
; }
;     ...
;             pv_d0(o, VB3(j - 1), pa0, pa1, pa2, pa3); partialSM<MODE>(pB0, pB1, m_reg, mnB, alB);
;             RESC(alB); VM_WAIT(); __syncthreads();
	v_mfma_f32_32x32x16_bf16 v[48:63], v[126:129], v[164:167], v[48:63]
	ds_read_b64_tr_b16 v[164:165], v138 offset:0x400
	ds_read_b64_tr_b16 v[166:167], v138 offset:0xc00
	v_mfma_f32_32x32x16_bf16 v[48:63], v[130:133], v[168:171], v[48:63]
	ds_read_b64_tr_b16 v[168:169], v138 offset:0x1400
	ds_read_b64_tr_b16 v[170:171], v138 offset:0x1c00
	v_mfma_f32_32x32x16_bf16 v[48:63], v[134:137], v[172:175], v[48:63]
	ds_read_b64_tr_b16 v[172:173], v138 offset:0x2400
	ds_read_b64_tr_b16 v[174:175], v138 offset:0x2c00
	v_mfma_f32_32x32x16_bf16 v[48:63], v[160:163], v[176:179], v[48:63]
	ds_read_b64_tr_b16 v[176:177], v138 offset:0x3400
	ds_read_b64_tr_b16 v[178:179], v138 offset:0x3c00
	s_waitcnt lgkmcnt(0)
	v_mfma_f32_32x32x16_bf16 v[32:47], v[126:129], v[164:167], v[32:47]
	ds_read_b64_tr_b16 v[164:165], v138 offset:0x600
	ds_read_b64_tr_b16 v[166:167], v138 offset:0xe00
	v_mfma_f32_32x32x16_bf16 v[32:47], v[130:133], v[168:171], v[32:47]
	ds_read_b64_tr_b16 v[168:169], v138 offset:0x1600
	ds_read_b64_tr_b16 v[170:171], v138 offset:0x1e00
	v_mfma_f32_32x32x16_bf16 v[32:47], v[134:137], v[172:175], v[32:47]
	ds_read_b64_tr_b16 v[172:173], v138 offset:0x2600
	ds_read_b64_tr_b16 v[174:175], v138 offset:0x2e00
	v_mfma_f32_32x32x16_bf16 v[32:47], v[160:163], v[176:179], v[32:47]
	ds_read_b64_tr_b16 v[176:177], v138 offset:0x3600
	ds_read_b64_tr_b16 v[178:179], v138 offset:0x3e00
	s_waitcnt lgkmcnt(0)
	v_mfma_f32_32x32x16_bf16 v[16:31], v[126:129], v[164:167], v[16:31]
	v_max_f32_e32 v126, v81, v81
	v_max_f32_e32 v127, v80, v80
	v_max_f32_e32 v126, v127, v126
	v_max3_f32 v126, v126, v82, v83
	v_max3_f32 v126, v126, v84, v85
	v_max3_f32 v126, v126, v86, v87
	v_max3_f32 v126, v126, v88, v89
	v_max3_f32 v126, v126, v90, v91
	v_max3_f32 v126, v126, v92, v93
	v_mfma_f32_32x32x16_bf16 v[16:31], v[130:133], v[168:171], v[16:31]
	v_max3_f32 v126, v126, v94, v95
	v_max3_f32 v126, v126, v64, v65
	v_max3_f32 v126, v126, v66, v67
	v_max3_f32 v126, v126, v68, v69
	v_max3_f32 v126, v126, v70, v71
	v_max3_f32 v126, v126, v72, v73
	v_max3_f32 v126, v126, v74, v75
	v_max3_f32 v126, v126, v76, v77
	v_mfma_f32_32x32x16_bf16 v[16:31], v[134:137], v[172:175], v[16:31]
	v_max3_f32 v126, v126, v78, v79
	v_mov_b32_e32 v127, v126
	s_nop 1
	v_permlane32_swap_b32_e32 v126, v127
	v_max_f32_e32 v127, v127, v127
	v_max_f32_e32 v126, v126, v126
	v_max_f32_e32 v126, v126, v127
	v_sub_f32_e32 v127, v126, v158
	v_cmp_ge_f32_e32 vcc, s17, v127
	v_max_f32_e32 v127, v158, v158
	v_max_f32_e32 v127, v127, v126
	v_mfma_f32_32x32x16_bf16 v[16:31], v[160:163], v[176:179], v[16:31]
	v_sub_f32_e32 v126, v158, v127
	v_mul_f32_e32 v126, 0x3e38aa3b, v126
	v_exp_f32_e32 v126, v126
	s_cmp_eq_u64 vcc, exec
	s_cselect_b64 s[4:5], -1, 0
	v_cndmask_b32_e64 v126, v126, 1.0, s[4:5]
	v_cmp_gt_f32_e32 vcc, 1.0, v126
	s_cbranch_vccz .LBB0_503
	s_and_saveexec_b64 s[0:1], s[2:3]
	ds_write_b32 v144, v126 offset:128
	s_or_b64 exec, exec, s[0:1]
	s_waitcnt lgkmcnt(0)
	v_add_u32_e32 v159, v143, v112
	ds_read_b128 v[128:131], v159 offset:224
	ds_read_b128 v[132:135], v159 offset:192
	ds_read_b128 v[136:139], v159 offset:160
	ds_read_b128 v[160:163], v159 offset:128
	s_waitcnt lgkmcnt(0)
	v_pk_mul_f32 v[12:13], v[12:13], v[128:129]
	v_pk_mul_f32 v[8:9], v[8:9], v[132:133]
	v_pk_mul_f32 v[4:5], v[4:5], v[136:137]
	v_pk_mul_f32 v[14:15], v[14:15], v[130:131]
	v_pk_mul_f32 v[10:11], v[10:11], v[134:135]
	v_pk_mul_f32 v[6:7], v[6:7], v[138:139]
	v_pk_mul_f32 v[2:3], v[2:3], v[162:163]
	v_pk_mul_f32 v[0:1], v[0:1], v[160:161]
	v_pk_mul_f32 v[60:61], v[60:61], v[128:129]
	v_pk_mul_f32 v[56:57], v[56:57], v[132:133]
	v_pk_mul_f32 v[52:53], v[52:53], v[136:137]
	v_pk_mul_f32 v[62:63], v[62:63], v[130:131]
	v_pk_mul_f32 v[58:59], v[58:59], v[134:135]
	v_pk_mul_f32 v[54:55], v[54:55], v[138:139]
	v_pk_mul_f32 v[50:51], v[50:51], v[162:163]
	v_pk_mul_f32 v[48:49], v[48:49], v[160:161]
	v_pk_mul_f32 v[44:45], v[44:45], v[128:129]
	v_pk_mul_f32 v[40:41], v[40:41], v[132:133]
	v_pk_mul_f32 v[36:37], v[36:37], v[136:137]
	v_pk_mul_f32 v[46:47], v[46:47], v[130:131]
	v_pk_mul_f32 v[42:43], v[42:43], v[134:135]
	v_pk_mul_f32 v[38:39], v[38:39], v[138:139]
	v_pk_mul_f32 v[34:35], v[34:35], v[162:163]
	v_pk_mul_f32 v[32:33], v[32:33], v[160:161]
	v_pk_mul_f32 v[28:29], v[28:29], v[128:129]
	v_pk_mul_f32 v[24:25], v[24:25], v[132:133]
	v_pk_mul_f32 v[20:21], v[20:21], v[136:137]
	v_pk_mul_f32 v[30:31], v[30:31], v[130:131]
	v_pk_mul_f32 v[26:27], v[26:27], v[134:135]
	v_pk_mul_f32 v[22:23], v[22:23], v[138:139]
	v_pk_mul_f32 v[18:19], v[18:19], v[162:163]
	v_pk_mul_f32 v[16:17], v[16:17], v[160:161]
.LBB0_503:
	s_add_i32 s0, s16, 4
	s_mul_i32 s1, s0, 0xab
	s_bfe_u32 s1, s1, 0x70009
	s_mul_i32 s1, s1, 3
	s_sub_i32 s0, s0, s1
	s_and_b32 s0, s0, 0xff
	v_cndmask_b32_e64 v127, v127, v158, s[4:5]
	s_lshl_b32 s1, s0, 14
	v_mul_f32_e32 v161, 0xbe38aa3b, v127
	s_add_i32 s1, s12, s1
	s_mulk_i32 s0, 0x6000
	v_fmamk_f32 v163, v64, 0x3e38aa3b, v161
	v_fmamk_f32 v184, v65, 0x3e38aa3b, v161
	s_add_i32 s0, s12, s0
	v_lshl_add_u64 v[64:65], v[118:119], 0, s[22:23]
	s_mov_b32 m0, s1
	s_cmp_eq_u32 s53, 12
	s_cbranch_scc1 .Lilc_w12_db
	s_cmp_eq_u32 s53, 8
	s_cbranch_scc1 .Lilc_w8_db
	s_waitcnt vmcnt(0)
	s_branch .Lilc_wd_db

; #define VM_WAIT() asm volatile("s_waitcnt vmcnt(0)" ::: "memory")
; #define SBAR() __builtin_amdgcn_sched_barrier(0)
; #define RESC(a) do { if (__any((a) < 1.f)) { if (hi == 0) al_l[r32] = (a); asm volatile("s_waitcnt lgkmcnt(0)" ::: "memory"); \
;         _Pragma("unroll") for (int d = 0; d < 4; ++d) _Pragma("unroll") for (int r = 0; r < 16; ++r) o[d][r] *= al_l[crow(r, hi)]; } } while (0)
; template <int MODE>
; __device__ __forceinline__ void partialSM(f32x16& p0, f32x16& p1, float& m_reg, float& mn, float& alpha) {
;     ...
;     const float mnC = -mn * C;
; #pragma unroll
;     for (int r = 0; r < 16; ++r) p0[r] = fmaf(p0[r], C, mnC);
; #pragma unroll
;     for (int r = 0; r < 16; ++r) p1[r] = fmaf(p1[r], C, mnC);
; #pragma unroll
;     for (int r = 0; r < 16; ++r) p0[r] = __builtin_amdgcn_exp2f(p0[r]);
; }
; __device__ __forceinline__ void finishSM(f32x16& p0, f32x16& p1, float alpha, float& l_reg, bf16x8& pa0, bf16x8& pa1, bf16x8& pa2, bf16x8& pa3) {
; #pragma unroll
;     for (int r = 0; r < 16; ++r) p1[r] = __builtin_amdgcn_exp2f(p1[r]);
;     float ps = 0;
; #pragma unroll
;     for (int r = 0; r < 16; ++r) ps += p0[r];
; #pragma unroll
;     for (int r = 0; r < 16; ++r) ps += p1[r];
;     { auto rr = __builtin_amdgcn_permlane32_swap(__float_as_uint(ps), __float_as_uint(ps), false, false);
;       ps = __uint_as_float(rr[0]) + __uint_as_float(rr[1]); }
;     l_reg = l_reg * alpha + ps;
;     ...
;     PK4(p0, 0, pa0); PK4(p0, 8, pa1); PK4(p1, 0, pa2); PK4(p1, 8, pa3);
;     ...
; }
;     ...
;             RESC(alB); VM_WAIT(); __syncthreads();
;             if (j + 2 < NT) GLDS3(j + 2);
;             SBAR(); qkt<MODE>(p0, p1, KB3(j + 1), qr, r32, hi);
;             finishSM(pB0, pB1, alB, l_reg, pa0, pa1, pa2, pa3); SBAR();
;             pv_d0(o, VB3(j), pa0, pa1, pa2, pa3); partialSM<MODE>(p0, p1, m_reg, mn, al);
.Lilc_wd_db:
	s_barrier
	s_add_i32 s4, s0, 0xc000
	global_load_lds_dwordx4 v[64:65], off
	v_lshl_add_u64 v[64:65], v[120:121], 0, s[22:23]
	s_add_i32 m0, s1, 0x2000
	s_mov_b64 s[0:1], 0x2981800
	global_load_lds_dwordx4 v[64:65], off
	v_lshl_add_u64 v[64:65], v[122:123], 0, s[0:1]
	s_mov_b32 m0, s4
	v_fmamk_f32 v80, v80, 0x3e38aa3b, v161
	global_load_lds_dwordx4 v[64:65], off
	v_fmamk_f32 v81, v81, 0x3e38aa3b, v161
	v_fmamk_f32 v82, v82, 0x3e38aa3b, v161
	v_fmamk_f32 v83, v83, 0x3e38aa3b, v161
	v_fmamk_f32 v84, v84, 0x3e38aa3b, v161
	v_fmamk_f32 v85, v85, 0x3e38aa3b, v161
	v_fmamk_f32 v86, v86, 0x3e38aa3b, v161
	v_fmamk_f32 v87, v87, 0x3e38aa3b, v161
	v_fmamk_f32 v88, v88, 0x3e38aa3b, v161
	v_fmamk_f32 v89, v89, 0x3e38aa3b, v161
	v_fmamk_f32 v90, v90, 0x3e38aa3b, v161
	v_fmamk_f32 v91, v91, 0x3e38aa3b, v161
	v_fmamk_f32 v92, v92, 0x3e38aa3b, v161
	v_fmamk_f32 v93, v93, 0x3e38aa3b, v161
	v_fmamk_f32 v94, v94, 0x3e38aa3b, v161
	v_fmamk_f32 v95, v95, 0x3e38aa3b, v161
	v_fmamk_f32 v185, v66, 0x3e38aa3b, v161
	v_fmamk_f32 v186, v67, 0x3e38aa3b, v161
	v_fmamk_f32 v187, v68, 0x3e38aa3b, v161
	v_fmamk_f32 v188, v69, 0x3e38aa3b, v161
	v_fmamk_f32 v189, v70, 0x3e38aa3b, v161
	v_fmamk_f32 v190, v71, 0x3e38aa3b, v161
	v_fmamk_f32 v191, v72, 0x3e38aa3b, v161
	v_fmamk_f32 v194, v73, 0x3e38aa3b, v161
	v_fmamk_f32 v195, v74, 0x3e38aa3b, v161
	v_fmamk_f32 v196, v75, 0x3e38aa3b, v161
	v_fmamk_f32 v197, v76, 0x3e38aa3b, v161
	v_fmamk_f32 v198, v77, 0x3e38aa3b, v161
	v_fmamk_f32 v199, v78, 0x3e38aa3b, v161
	v_fmac_f32_e32 v161, 0x3e38aa3b, v79
	v_exp_f32_e32 v136, v80
	v_exp_f32_e32 v137, v81
	v_exp_f32_e32 v138, v82
	v_exp_f32_e32 v139, v83
	v_exp_f32_e32 v158, v84
	v_exp_f32_e32 v159, v85
	v_exp_f32_e32 v160, v86
	v_exp_f32_e32 v162, v87
	v_exp_f32_e32 v128, v88
	v_exp_f32_e32 v129, v89
	v_exp_f32_e32 v130, v90
	v_exp_f32_e32 v131, v91
	v_exp_f32_e32 v132, v92
	v_exp_f32_e32 v133, v93
	v_exp_f32_e32 v134, v94
	v_exp_f32_e32 v135, v95
	v_add_u32_e32 v72, s15, v147
	v_add_u32_e32 v68, v72, v149
	v_add_u32_e32 v73, v72, v153
	ds_read_b128 v[64:67], v68 offset:49152
	ds_read_b128 v[68:71], v68 offset:53248
	ds_read_b128 v[118:121], v73 offset:49152
	ds_read_b128 v[164:167], v73 offset:53248
	v_add_u32_e32 v73, v72, v154
	ds_read_b128 v[168:171], v73 offset:49152
	ds_read_b128 v[172:175], v73 offset:53248
	s_waitcnt lgkmcnt(0)
	v_mfma_f32_32x32x16_bf16 v[80:95], v[64:67], v[104:107], 0
	v_add_u32_e32 v64, v72, v156
	ds_read_b128 v[176:179], v64 offset:49152
	ds_read_b128 v[180:183], v64 offset:53248
	v_mfma_f32_32x32x16_bf16 v[64:79], v[68:71], v[104:107], 0
	v_mfma_f32_32x32x16_bf16 v[80:95], v[118:121], v[108:111], v[80:95]
	v_mfma_f32_32x32x16_bf16 v[64:79], v[164:167], v[108:111], v[64:79]
	v_mfma_f32_32x32x16_bf16 v[80:95], v[168:171], v[100:103], v[80:95]
	v_mfma_f32_32x32x16_bf16 v[64:79], v[172:175], v[100:103], v[64:79]
	s_waitcnt lgkmcnt(0)
	v_mfma_f32_32x32x16_bf16 v[80:95], v[176:179], v[96:99], v[80:95]
	v_mfma_f32_32x32x16_bf16 v[64:79], v[180:183], v[96:99], v[64:79]
	v_add_f32_e32 v120, 0, v136
	v_add_f32_e32 v120, v137, v120
	v_add_f32_e32 v120, v138, v120
	v_add_f32_e32 v120, v139, v120
	v_add_f32_e32 v120, v158, v120
	v_add_f32_e32 v120, v159, v120
	v_add_f32_e32 v120, v160, v120
	v_add_f32_e32 v120, v162, v120
	v_add_f32_e32 v120, v128, v120
	v_add_f32_e32 v120, v129, v120
	v_add_f32_e32 v120, v130, v120
	v_add_f32_e32 v120, v131, v120
	v_exp_f32_e32 v118, v163
	v_add_f32_e32 v120, v132, v120
	v_exp_f32_e32 v119, v184
	v_add_f32_e32 v120, v133, v120
	v_exp_f32_e32 v122, v185
	v_add_f32_e32 v120, v134, v120
	v_exp_f32_e32 v123, v186
	v_add_f32_e32 v120, v135, v120
	v_exp_f32_e32 v163, v187
	v_add_f32_e32 v120, v118, v120
	v_exp_f32_e32 v164, v188
	v_add_f32_e32 v120, v119, v120
	v_exp_f32_e32 v165, v189
	v_add_f32_e32 v120, v122, v120
	v_exp_f32_e32 v166, v190
	v_add_f32_e32 v120, v123, v120
	v_exp_f32_e32 v167, v191
	v_add_f32_e32 v120, v163, v120
	v_exp_f32_e32 v168, v194
	v_add_f32_e32 v120, v164, v120
	v_exp_f32_e32 v169, v195
	v_add_f32_e32 v120, v165, v120
	v_exp_f32_e32 v170, v196
	v_add_f32_e32 v120, v166, v120
	v_exp_f32_e32 v171, v197
	v_add_f32_e32 v120, v167, v120
	v_exp_f32_e32 v172, v198
	v_add_f32_e32 v120, v168, v120
	v_exp_f32_e32 v173, v199
	v_add_f32_e32 v120, v169, v120
	v_exp_f32_e32 v161, v161
	v_add_f32_e32 v120, v170, v120
	v_add_f32_e32 v120, v171, v120
	v_add_f32_e32 v120, v172, v120
	v_add_f32_e32 v120, v173, v120
	v_add_f32_e32 v120, v161, v120
	v_mov_b32_e32 v121, v120
	s_nop 1
	v_permlane32_swap_b32_e32 v120, v121
	v_cvt_pk_bf16_f32 v136, v136, v137
	v_cvt_pk_bf16_f32 v137, v138, v139
	v_cvt_pk_bf16_f32 v138, v158, v159
	v_cvt_pk_bf16_f32 v139, v160, v162
	v_cvt_pk_bf16_f32 v128, v128, v129
	v_cvt_pk_bf16_f32 v129, v130, v131
	v_cvt_pk_bf16_f32 v130, v132, v133
	v_cvt_pk_bf16_f32 v131, v134, v135
	v_cvt_pk_bf16_f32 v132, v118, v119
	v_cvt_pk_bf16_f32 v133, v122, v123
	v_cvt_pk_bf16_f32 v134, v163, v164
	v_cvt_pk_bf16_f32 v135, v165, v166
	v_cvt_pk_bf16_f32 v158, v167, v168
	v_cvt_pk_bf16_f32 v159, v169, v170
	v_cvt_pk_bf16_f32 v160, v171, v172
	v_cvt_pk_bf16_f32 v161, v173, v161
	s_nop 0
	v_permlane32_swap_b32_e32 v136, v138
	v_permlane32_swap_b32_e32 v137, v139
	v_permlane32_swap_b32_e32 v128, v130
	v_permlane32_swap_b32_e32 v129, v131
	v_permlane32_swap_b32_e32 v132, v134
	v_permlane32_swap_b32_e32 v133, v135
	v_permlane32_swap_b32_e32 v158, v160
	v_permlane32_swap_b32_e32 v159, v161
	v_lshl_add_u32 v118, s14, 14, v113
	ds_read_b64_tr_b16 v[162:163], v118 offset:0
	ds_read_b64_tr_b16 v[164:165], v118 offset:0x800
	ds_read_b64_tr_b16 v[166:167], v118 offset:0x1000
	ds_read_b64_tr_b16 v[168:169], v118 offset:0x1800
	ds_read_b64_tr_b16 v[170:171], v118 offset:0x2000
	ds_read_b64_tr_b16 v[172:173], v118 offset:0x2800
	ds_read_b64_tr_b16 v[174:175], v118 offset:0x3000
	ds_read_b64_tr_b16 v[176:177], v118 offset:0x3800
	s_waitcnt lgkmcnt(0)
; #define VM_WAIT() asm volatile("s_waitcnt vmcnt(0)" ::: "memory")
; #define SBAR() __builtin_amdgcn_sched_barrier(0)
; #define RESC(a) do { if (__any((a) < 1.f)) { if (hi == 0) al_l[r32] = (a); asm volatile("s_waitcnt lgkmcnt(0)" ::: "memory"); \
;         _Pragma("unroll") for (int d = 0; d < 4; ++d) _Pragma("unroll") for (int r = 0; r < 16; ++r) o[d][r] *= al_l[crow(r, hi)]; } } while (0)
; template <int D0> __device__ __forceinline__ void pv_one(f32x16& od, int vb, bf16x8 pa0, bf16x8 pa1, bf16x8 pa2, bf16x8 pa3) {
;     const s16x4 l0 = tr_read<v_rd_off(D0, 0, 0)>(vb), h0 = tr_read<v_rd_off(D0, 0, 1)>(vb), l1 = tr_read<v_rd_off(D0, 1, 0)>(vb), h1 = tr_read<v_rd_off(D0, 1, 1)>(vb);
;     const s16x4 l2 = tr_read<v_rd_off(D0, 2, 0)>(vb), h2 = tr_read<v_rd_off(D0, 2, 1)>(vb), l3 = tr_read<v_rd_off(D0, 3, 0)>(vb), h3 = tr_read<v_rd_off(D0, 3, 1)>(vb);
;     asm volatile("s_waitcnt lgkmcnt(0)" ::: "memory"); SBAR();
;     ...
;     od = __builtin_amdgcn_mfma_f32_32x32x16_bf16(pa0, PK(l0, h0), od, 0, 0, 0);
;     od = __builtin_amdgcn_mfma_f32_32x32x16_bf16(pa1, PK(l1, h1), od, 0, 0, 0);
;     od = __builtin_amdgcn_mfma_f32_32x32x16_bf16(pa2, PK(l2, h2), od, 0, 0, 0);
;     od = __builtin_amdgcn_mfma_f32_32x32x16_bf16(pa3, PK(l3, h3), od, 0, 0, 0);
;     ...
; }
; __device__ __forceinline__ void pv_d0(f32x16* o, int vb, bf16x8 pa0, bf16x8 pa1, bf16x8 pa2, bf16x8 pa3) {
;     pv_one<0>(o[0], vb, pa0, pa1, pa2, pa3); pv_one<1>(o[1], vb, pa0, pa1, pa2, pa3); pv_one<2>(o[2], vb, pa0, pa1, pa2, pa3); pv_one<3>(o[3], vb, pa0, pa1, pa2, pa3);
; }
;     ...
;             pv_d0(o, VB3(j), pa0, pa1, pa2, pa3); partialSM<MODE>(p0, p1, m_reg, mn, al);
;             RESC(al); VM_WAIT(); __syncthreads();
	s_nop 0
	v_mfma_f32_32x32x16_bf16 v[0:15], v[136:139], v[162:165], v[0:15]
	ds_read_b64_tr_b16 v[162:163], v118 offset:0x200
	ds_read_b64_tr_b16 v[164:165], v118 offset:0xa00
	v_mfma_f32_32x32x16_bf16 v[0:15], v[128:131], v[166:169], v[0:15]
	ds_read_b64_tr_b16 v[166:167], v118 offset:0x1200
	ds_read_b64_tr_b16 v[168:169], v118 offset:0x1a00
	v_mfma_f32_32x32x16_bf16 v[0:15], v[132:135], v[170:173], v[0:15]
	ds_read_b64_tr_b16 v[170:171], v118 offset:0x2200
	ds_read_b64_tr_b16 v[172:173], v118 offset:0x2a00
	v_mfma_f32_32x32x16_bf16 v[0:15], v[158:161], v[174:177], v[0:15]
	ds_read_b64_tr_b16 v[174:175], v118 offset:0x3200
	ds_read_b64_tr_b16 v[176:177], v118 offset:0x3a00
	s_waitcnt lgkmcnt(0)
	v_mfma_f32_32x32x16_bf16 v[48:63], v[136:139], v[162:165], v[48:63]
	ds_read_b64_tr_b16 v[162:163], v118 offset:0x400
	ds_read_b64_tr_b16 v[164:165], v118 offset:0xc00
	v_mfma_f32_32x32x16_bf16 v[48:63], v[128:131], v[166:169], v[48:63]
	ds_read_b64_tr_b16 v[166:167], v118 offset:0x1400
	ds_read_b64_tr_b16 v[168:169], v118 offset:0x1c00
	v_mfma_f32_32x32x16_bf16 v[48:63], v[132:135], v[170:173], v[48:63]
	ds_read_b64_tr_b16 v[170:171], v118 offset:0x2400
	ds_read_b64_tr_b16 v[172:173], v118 offset:0x2c00
	v_mfma_f32_32x32x16_bf16 v[48:63], v[158:161], v[174:177], v[48:63]
	ds_read_b64_tr_b16 v[174:175], v118 offset:0x3400
	ds_read_b64_tr_b16 v[176:177], v118 offset:0x3c00
	s_waitcnt lgkmcnt(0)
	v_mfma_f32_32x32x16_bf16 v[32:47], v[136:139], v[162:165], v[32:47]
	ds_read_b64_tr_b16 v[162:163], v118 offset:0x600
	ds_read_b64_tr_b16 v[164:165], v118 offset:0xe00
	v_mfma_f32_32x32x16_bf16 v[32:47], v[128:131], v[166:169], v[32:47]
	ds_read_b64_tr_b16 v[166:167], v118 offset:0x1600
	ds_read_b64_tr_b16 v[168:169], v118 offset:0x1e00
	v_mfma_f32_32x32x16_bf16 v[32:47], v[132:135], v[170:173], v[32:47]
	ds_read_b64_tr_b16 v[170:171], v118 offset:0x2600
	ds_read_b64_tr_b16 v[172:173], v118 offset:0x2e00
	v_mfma_f32_32x32x16_bf16 v[32:47], v[158:161], v[174:177], v[32:47]
	ds_read_b64_tr_b16 v[174:175], v118 offset:0x3600
	ds_read_b64_tr_b16 v[176:177], v118 offset:0x3e00
	s_waitcnt lgkmcnt(0)
	v_mfma_f32_32x32x16_bf16 v[16:31], v[136:139], v[162:165], v[16:31]
	v_max_f32_e32 v118, v81, v81
	v_max_f32_e32 v119, v80, v80
	v_max_f32_e32 v118, v119, v118
	v_max3_f32 v118, v118, v82, v83
	v_max3_f32 v118, v118, v84, v85
	v_max3_f32 v118, v118, v86, v87
	v_max3_f32 v118, v118, v88, v89
	v_max3_f32 v118, v118, v90, v91
	v_max3_f32 v118, v118, v92, v93
	v_mfma_f32_32x32x16_bf16 v[16:31], v[128:131], v[166:169], v[16:31]
	v_max3_f32 v118, v118, v94, v95
	v_max3_f32 v118, v118, v64, v65
	v_max3_f32 v118, v118, v66, v67
	v_max3_f32 v118, v118, v68, v69
	v_max3_f32 v118, v118, v70, v71
	v_max3_f32 v118, v118, v72, v73
	v_max3_f32 v118, v118, v74, v75
	v_max3_f32 v118, v118, v76, v77
	v_mfma_f32_32x32x16_bf16 v[16:31], v[132:135], v[170:173], v[16:31]
	v_max3_f32 v118, v118, v78, v79
	v_mov_b32_e32 v119, v118
	s_nop 1
	v_permlane32_swap_b32_e32 v118, v119
	v_max_f32_e32 v119, v119, v119
	v_max_f32_e32 v118, v118, v118
	v_max_f32_e32 v118, v118, v119
	v_sub_f32_e32 v119, v118, v127
	v_cmp_ge_f32_e32 vcc, s17, v119
	v_max_f32_e32 v119, v127, v127
	v_max_f32_e32 v118, v119, v118
	v_mfma_f32_32x32x16_bf16 v[16:31], v[158:161], v[174:177], v[16:31]
	v_sub_f32_e32 v119, v127, v118
	v_mul_f32_e32 v119, 0x3e38aa3b, v119
	v_exp_f32_e32 v119, v119
	s_cmp_eq_u64 vcc, exec
	s_cselect_b64 s[4:5], -1, 0
	v_cndmask_b32_e64 v119, v119, 1.0, s[4:5]
	v_cmp_gt_f32_e32 vcc, 1.0, v119
	s_cbranch_vccz .LBB0_507
	s_and_saveexec_b64 s[0:1], s[2:3]
	ds_write_b32 v144, v119 offset:128
	s_or_b64 exec, exec, s[0:1]
	s_waitcnt lgkmcnt(0)
	v_add_u32_e32 v122, v143, v112
	ds_read_b128 v[128:131], v122 offset:224
	ds_read_b128 v[132:135], v122 offset:192
	ds_read_b128 v[136:139], v122 offset:160
	ds_read_b128 v[158:161], v122 offset:128
	s_waitcnt lgkmcnt(0)
	v_pk_mul_f32 v[12:13], v[12:13], v[128:129]
	v_pk_mul_f32 v[8:9], v[8:9], v[132:133]
	v_pk_mul_f32 v[4:5], v[4:5], v[136:137]
	v_pk_mul_f32 v[14:15], v[14:15], v[130:131]
	v_pk_mul_f32 v[10:11], v[10:11], v[134:135]
	v_pk_mul_f32 v[6:7], v[6:7], v[138:139]
	v_pk_mul_f32 v[2:3], v[2:3], v[160:161]
	v_pk_mul_f32 v[0:1], v[0:1], v[158:159]
	v_pk_mul_f32 v[60:61], v[60:61], v[128:129]
	v_pk_mul_f32 v[56:57], v[56:57], v[132:133]
	v_pk_mul_f32 v[52:53], v[52:53], v[136:137]
	v_pk_mul_f32 v[62:63], v[62:63], v[130:131]
	v_pk_mul_f32 v[58:59], v[58:59], v[134:135]
	v_pk_mul_f32 v[54:55], v[54:55], v[138:139]
	v_pk_mul_f32 v[50:51], v[50:51], v[160:161]
	v_pk_mul_f32 v[48:49], v[48:49], v[158:159]
	v_pk_mul_f32 v[44:45], v[44:45], v[128:129]
	v_pk_mul_f32 v[40:41], v[40:41], v[132:133]
	v_pk_mul_f32 v[36:37], v[36:37], v[136:137]
	v_pk_mul_f32 v[46:47], v[46:47], v[130:131]
	v_pk_mul_f32 v[42:43], v[42:43], v[134:135]
	v_pk_mul_f32 v[38:39], v[38:39], v[138:139]
	v_pk_mul_f32 v[34:35], v[34:35], v[160:161]
	v_pk_mul_f32 v[32:33], v[32:33], v[158:159]
	v_pk_mul_f32 v[28:29], v[28:29], v[128:129]
	v_pk_mul_f32 v[24:25], v[24:25], v[132:133]
	v_pk_mul_f32 v[20:21], v[20:21], v[136:137]
	v_pk_mul_f32 v[30:31], v[30:31], v[130:131]
	v_pk_mul_f32 v[26:27], v[26:27], v[134:135]
	v_pk_mul_f32 v[22:23], v[22:23], v[138:139]
	v_pk_mul_f32 v[18:19], v[18:19], v[160:161]
	v_pk_mul_f32 v[16:17], v[16:17], v[158:159]

; #define LAS __attribute__((address_space(3)))
; __device__ __forceinline__ float clamp8(float x) { return __builtin_amdgcn_fmed3f(x, -448.f, 448.f); }
; __device__ __forceinline__ void cvt_finish(const CvtDesc& d, const float (&t)[64], LAS float* scr, int lane) {
;     ...
;     if (d.f8) {
; #pragma unroll
;         for (int j = 0; j < 8; ++j) { const int n = (lane >> 3) + 8 * j; const LAS float* s = scr + (8 * c) * 65 + n;
;             int a = __builtin_amdgcn_cvt_pk_fp8_f32(clamp8(s[0 * 65] * W8_SCALE), clamp8(s[1 * 65] * W8_SCALE), 0, false); a = __builtin_amdgcn_cvt_pk_fp8_f32(clamp8(s[2 * 65] * W8_SCALE), clamp8(s[3 * 65] * W8_SCALE), a, true);
;             int b = __builtin_amdgcn_cvt_pk_fp8_f32(clamp8(s[4 * 65] * W8_SCALE), clamp8(s[5 * 65] * W8_SCALE), 0, false); b = __builtin_amdgcn_cvt_pk_fp8_f32(clamp8(s[6 * 65] * W8_SCALE), clamp8(s[7 * 65] * W8_SCALE), b, true);
;             __builtin_nontemporal_store((u32x2){(unsigned)a, (unsigned)b}, (u32x2*)(d.dst + (size_t)n * d.dKB + 8 * c)); }
.LBB0_509:
	s_cmp_eq_u32 s42, 0
	s_cbranch_scc1 .Lilc_fd_da
	v_mul_f32_e32 v232, 0x42800000, v232
	v_mul_f32_e32 v233, 0x42800000, v233
	v_mul_f32_e32 v234, 0x42800000, v234
	v_mul_f32_e32 v235, 0x42800000, v235
	v_mul_f32_e32 v236, 0x42800000, v236
	v_mul_f32_e32 v237, 0x42800000, v237
	v_mul_f32_e32 v238, 0x42800000, v238
	v_mul_f32_e32 v239, 0x42800000, v239
	v_mul_f32_e32 v240, 0x42800000, v240
	v_mul_f32_e32 v241, 0x42800000, v241
	v_mul_f32_e32 v242, 0x42800000, v242
	v_mul_f32_e32 v243, 0x42800000, v243
	v_mul_f32_e32 v244, 0x42800000, v244
	v_mul_f32_e32 v245, 0x42800000, v245
	v_mul_f32_e32 v246, 0x42800000, v246
	v_mul_f32_e32 v247, 0x42800000, v247
	v_mul_f32_e32 v248, 0x42800000, v248
	v_mul_f32_e32 v249, 0x42800000, v249
	v_mul_f32_e32 v250, 0x42800000, v250
	v_mul_f32_e32 v251, 0x42800000, v251
	v_mul_f32_e32 v206, 0x42800000, v206
	v_mul_f32_e32 v207, 0x42800000, v207
	v_mul_f32_e32 v208, 0x42800000, v208
	v_mul_f32_e32 v209, 0x42800000, v209
	v_mul_f32_e32 v210, 0x42800000, v210
	v_mul_f32_e32 v211, 0x42800000, v211
	v_mul_f32_e32 v212, 0x42800000, v212
	v_mul_f32_e32 v213, 0x42800000, v213
	v_mul_f32_e32 v214, 0x42800000, v214
	v_mul_f32_e32 v215, 0x42800000, v215
	v_mul_f32_e32 v216, 0x42800000, v216
	v_mul_f32_e32 v217, 0x42800000, v217
	v_med3_f32 v232, v232, s93, v224
	v_med3_f32 v233, v233, s93, v224
	v_med3_f32 v234, v234, s93, v224
	v_med3_f32 v235, v235, s93, v224
	v_med3_f32 v236, v236, s93, v224
	v_med3_f32 v237, v237, s93, v224
	v_med3_f32 v238, v238, s93, v224
	v_med3_f32 v239, v239, s93, v224
	v_med3_f32 v240, v240, s93, v224
	v_med3_f32 v241, v241, s93, v224
	v_med3_f32 v242, v242, s93, v224
	v_med3_f32 v243, v243, s93, v224
	v_med3_f32 v244, v244, s93, v224
	v_med3_f32 v245, v245, s93, v224
	v_med3_f32 v246, v246, s93, v224
	v_med3_f32 v247, v247, s93, v224
	v_med3_f32 v248, v248, s93, v224
	v_med3_f32 v249, v249, s93, v224
	v_med3_f32 v250, v250, s93, v224
	v_med3_f32 v251, v251, s93, v224
	v_med3_f32 v206, v206, s93, v224
	v_med3_f32 v207, v207, s93, v224
	v_med3_f32 v208, v208, s93, v224
	v_med3_f32 v209, v209, s93, v224
	v_med3_f32 v210, v210, s93, v224
	v_med3_f32 v211, v211, s93, v224
	v_med3_f32 v212, v212, s93, v224
	v_med3_f32 v213, v213, s93, v224
	v_med3_f32 v214, v214, s93, v224
	v_med3_f32 v215, v215, s93, v224
	v_med3_f32 v216, v216, s93, v224
	v_med3_f32 v217, v217, s93, v224
	v_lshlrev_b32_e32 v230, 3, v226
	v_lshl_add_u32 v225, v229, s42, v230
	v_cvt_pk_fp8_f32 v252, v232, v236
	v_cvt_pk_fp8_f32 v253, v248, v206
	v_cvt_pk_fp8_f32 v252, v240, v244 op_sel:[0,0,1]
	v_cvt_pk_fp8_f32 v253, v210, v214 op_sel:[0,0,1]
	s_nop 0
	global_store_dwordx2 v225, v[252:253], s[40:41]
	v_add_u32_e32 v225, s43, v225
	v_cvt_pk_fp8_f32 v252, v233, v237
	v_cvt_pk_fp8_f32 v253, v249, v207
	v_cvt_pk_fp8_f32 v252, v241, v245 op_sel:[0,0,1]
	v_cvt_pk_fp8_f32 v253, v211, v215 op_sel:[0,0,1]
	s_nop 0
	global_store_dwordx2 v225, v[252:253], s[40:41]
	v_add_u32_e32 v225, s43, v225
	v_cvt_pk_fp8_f32 v252, v234, v238
	v_cvt_pk_fp8_f32 v253, v250, v208
	v_cvt_pk_fp8_f32 v252, v242, v246 op_sel:[0,0,1]
	v_cvt_pk_fp8_f32 v253, v212, v216 op_sel:[0,0,1]
	s_nop 0
	global_store_dwordx2 v225, v[252:253], s[40:41]
	v_add_u32_e32 v225, s43, v225
	v_cvt_pk_fp8_f32 v252, v235, v239
	v_cvt_pk_fp8_f32 v253, v251, v209
	v_cvt_pk_fp8_f32 v252, v243, v247 op_sel:[0,0,1]
	v_cvt_pk_fp8_f32 v253, v213, v217 op_sel:[0,0,1]
	s_nop 0
	global_store_dwordx2 v225, v[252:253], s[40:41]
	s_mov_b32 s42, 0

;     ...
;     int tid = tid_x(); asm volatile("" : "+v"(tid));
;     const int wid = tid >> 6, lane = tid & 63, r32 = lane & 31, hi = lane >> 5;
;     const int qb = uid & 15, h = (uid >> 4) % NH, b = (uid >> 4) / NH;
;     const int tok0 = b * SEQ;
;     const int qrow = tok0 + qb * 256 + wid * 32 + r32;
;     LAS char* V_lds = lds + LDS_VBUF; LAS char* K_lds = lds + LDS_KBUF;
;     LAS float* ws = (LAS float*)(lds + LDS_WS) + wid * 64; LAS float* li_l = ws; LAS float* al_l = ws + 32;
;     LAS float* rpbL = (LAS float*)(lds + LDS_RPB);
;     const int sr = tid >> 4, sc = (tid & 15) * 8, vst0 = v_st(sr, sc), vst1 = v_st(32 + sr, sc);
;     const int sr64 = tid >> 3, sc64 = (tid & 7) * 8;
;     const int vb0 = (int)(unsigned)(uintptr_t)V_lds + v_rd_base(lane);
;     int NT = 64, kbase = tok0;
;     int rq = 0, qc = 0, kr_lo = 0;
;     if constexpr (MODE == MODE_NA) { const int rq0 = qb * 4; kr_lo = min(min(max(rq0 - 4, 0), 56), 52); NT = 12; kbase = tok0 + kr_lo * 64; rq = rq0 + (wid >> 1); qc = (wid & 1) * 32 + r32;
;         for (int i = tid; i < 15 * 31; i += 512) rpbL[i] = P.rpb[h * 465 + i];
;         __syncthreads(); }
;     const bf16* Kg; const bf16* Vg; const bf16* Kg2 = nullptr; int ldk, ldv;
;     if constexpr (MODE == MODE_MLA) { Kg = P.KVM + h * 256; Vg = P.KVM + h * 256 + 128; Kg2 = P.U + U_KR; ldk = KVW; ldv = KVW; }
;     else if constexpr (MODE == MODE_NA) { Kg = P.U + U_NA + 512 + h * 128; Vg = P.U + U_NA + 1024 + h * 128; ldk = UW; ldv = UW; }
;     else { Kg = P.U + U_DF + 512 + h * 128; Vg = P.U + U_DF + 1024 + h * 128; ldk = UW; ldv = UW; }
;     constexpr int pass = PASS;
;     constexpr bool HALF_OFFSET = false;
;     {
;         float m_reg = -1e30f, l_reg = 0; f32x16 o[4] = {}; bf16x8 qr[NQ];
;         if constexpr (MODE == MODE_MLA) {
;             const bf16* Qw = P.QM + (size_t)qrow * QMW + h * 192 + hi * 8;
; #pragma unroll
;             for (int d0 = 0; d0 < 12; ++d0) qr[d0] = *(const bf16x8*)(Qw + d0 * 16);
;             const f32x2* rt = P.ropeM + (size_t)(qrow & (SEQ - 1)) * 32;
; #pragma unroll
;             for (int g = 0; g < 2; ++g) {
;                 bf16x8 x1 = qr[8 + g], x2 = qr[10 + g];
; #pragma unroll
;                 for (int e = 0; e < 8; ++e) { const f32x2 cs = rt[g * 16 + hi * 8 + e];
;                     const float a = bf2f((unsigned short)x1[e]), c = bf2f((unsigned short)x2[e]);
.LBB0_785:
	s_lshl_b32 s0, s22, 1
	s_and_b32 s0, s0, 14
	s_ashr_i32 s1, s22, 7
	s_add_i32 s0, s0, s1
	s_getreg_b32 s1, hwreg(HW_REG_HW_ID, 0, 6)
	s_and_b32 s1, s1, 63
	s_lshl_b32 s1, s1, 2
	s_add_i32 s1, s1, 0
	s_add_i32 s1, s1, 0x23f00
	s_waitcnt vmcnt(15)
	v_mov_b32_e32 v0, s1
	ds_read_b32 v0, v0
	v_mbcnt_lo_u32_b32 v1, -1, 0
	v_mbcnt_hi_u32_b32 v1, -1, v1
	v_mov_b32_e32 v145, v193
	v_mov_b32_e32 v149, v193
	s_movk_i32 s3, 0x70
	s_waitcnt lgkmcnt(0)
	v_readfirstlane_b32 s1, v0
	s_mov_b32 s28, 0
	s_and_b32 s39, s74, 63
	s_lshl_b32 s39, s39, 3
	s_add_u32 s39, s39, s1
	s_lshr_b32 s54, s74, 6
	v_lshrrev_b32_e32 v226, 3, v1
	v_and_b32_e32 v229, 7, v1
	v_readlane_b32 s56, v254, 60
	s_lshr_b32 s52, s1, 2
	s_mul_i32 s52, s52, 31
	s_add_u32 s52, s52, 31
	s_mov_b32 s42, 0
	s_mov_b32 s51, 16
	s_mov_b32 s53, 0
	v_mov_b32_e32 v147, v193
	s_waitcnt vmcnt(13)
	v_lshl_add_u32 v11, s1, 6, v1
	s_lshr_b32 s1, s0, 29
	s_add_i32 s1, s0, s1
	s_and_b32 s2, s1, -8
	s_sub_i32 s23, s0, s2
	s_lshl_b32 s0, s1, 9
	s_and_b32 s4, s0, 0xfffff000
	s_lshl_b32 s0, s22, 5
	s_and_b32 s0, s0, 0xf00
	s_or_b32 s25, s4, s0
	v_ashrrev_i32_e32 v156, 6, v11
	v_and_b32_e32 v154, 31, v11
	v_lshl_add_u32 v0, v156, 5, s25
	v_or_b32_e32 v8, v0, v154
	v_and_b32_e32 v0, 0x3fffffc0, v11
	s_add_i32 s0, 0, 0x1e000
	v_lshl_add_u32 v157, v0, 2, s0
	s_lshl_b32 s0, s23, 8
	s_ashr_i32 s1, s0, 31
	s_lshl_b64 s[0:1], s[0:1], 1
	s_add_u32 s26, s18, s0
	v_mov_b64_e32 v[0:1], s[10:11]
	s_movk_i32 s0, 0xc00
	s_addc_u32 s27, s19, s1
	v_mad_i64_i32 v[0:1], s[0:1], v8, s0, v[0:1]
	s_mul_i32 s0, s23, 0xc0
	v_lshlrev_b32_e32 v8, 8, v8
	v_bfe_u32 v155, v11, 5, 1
	s_ashr_i32 s1, s0, 31
	v_and_b32_e32 v192, 0xfff00, v8
	v_lshl_add_u64 v[0:1], s[0:1], 1, v[0:1]
	v_lshlrev_b32_e32 v144, 4, v155
	v_lshl_add_u64 v[8:9], s[12:13], 0, v[192:193]
	v_lshlrev_b32_e32 v192, 6, v155
	v_lshl_add_u64 v[4:5], v[0:1], 0, v[144:145]
	v_lshl_add_u64 v[8:9], v[8:9], 0, v[192:193]
	global_load_dwordx4 v[96:99], v[4:5], off
	global_load_dwordx4 v[100:103], v[4:5], off offset:32
	global_load_dwordx4 v[104:107], v[4:5], off offset:64
	global_load_dwordx4 v[108:111], v[4:5], off offset:96
	global_load_dwordx4 v[112:115], v[4:5], off offset:128
	global_load_dwordx4 v[116:119], v[4:5], off offset:160
	global_load_dwordx4 v[120:123], v[4:5], off offset:192
	global_load_dwordx4 v[124:127], v[4:5], off offset:224
	global_load_dwordx4 v[26:29], v[4:5], off offset:256
	global_load_dwordx4 v[0:3], v[4:5], off offset:288
	global_load_dwordx4 v[30:33], v[4:5], off offset:320
	s_nop 0
	global_load_dwordx4 v[4:7], v[4:5], off offset:352
	s_waitcnt vmcnt(24)
	v_lshlrev_b32_e32 v13, 4, v11
	global_load_dwordx2 v[14:15], v[8:9], off
	v_readfirstlane_b32 s0, v156
	s_ashr_i32 s5, s4, 31
	s_lshl_b32 s2, s0, 10
	s_lshl_b64 s[0:1], s[4:5], 12
	s_add_u32 s0, s26, s0
	s_addc_u32 s1, s27, s1
	s_add_i32 s29, s2, 0
	s_mov_b32 m0, s29
	s_add_i32 s2, s29, 0xc000
	v_and_b32_e32 v10, 63, v11
	v_and_b32_e32 v12, 0xc0, v13
	v_mov_b32_e32 v151, v193
	v_lshlrev_b32_e32 v145, 8, v154
	v_lshlrev_b32_e32 v167, 7, v154
	v_lshl_add_u32 v163, v154, 2, v157
	v_mov_b32_e32 v174, 0
	v_mov_b32_e32 v173, 0xf149f2ca
	s_waitcnt vmcnt(4)
	v_lshlrev_b32_e32 v17, 16, v26
	s_waitcnt vmcnt(2)
	v_lshlrev_b32_e32 v16, 16, v30
	s_waitcnt vmcnt(0)
	v_pk_mul_f32 v[18:19], v[14:15], v[16:17] op_sel:[0,1] op_sel_hi:[1,0]
	v_pk_mul_f32 v[14:15], v[14:15], v[16:17]
	v_sub_f32_e32 v18, v18, v19
	v_add_f32_e32 v14, v15, v14
	v_cvt_pk_bf16_f32 v15, v18, v193
	v_cvt_pk_bf16_f32 v14, v14, v193
	global_load_dwordx2 v[16:17], v[8:9], off offset:8
	v_and_b32_e32 v19, 0xffff0000, v26
	v_and_b32_e32 v18, 0xffff0000, v30
	s_waitcnt vmcnt(0)
	v_pk_mul_f32 v[20:21], v[16:17], v[18:19] op_sel:[0,1] op_sel_hi:[1,0]
	v_pk_mul_f32 v[16:17], v[16:17], v[18:19]
	v_sub_f32_e32 v20, v20, v21
	v_add_f32_e32 v16, v16, v17
	v_cvt_pk_bf16_f32 v17, v20, v193
	v_cvt_pk_bf16_f32 v16, v16, v193
	global_load_dwordx2 v[18:19], v[8:9], off offset:16
	v_lshlrev_b32_e32 v21, 16, v27
	v_lshlrev_b32_e32 v20, 16, v31
	s_waitcnt vmcnt(0)
	v_pk_mul_f32 v[22:23], v[18:19], v[20:21] op_sel:[0,1] op_sel_hi:[1,0]
	v_pk_mul_f32 v[18:19], v[18:19], v[20:21]
	v_sub_f32_e32 v22, v22, v23
	v_add_f32_e32 v18, v18, v19
	v_cvt_pk_bf16_f32 v19, v22, v193
	v_cvt_pk_bf16_f32 v18, v18, v193
	global_load_dwordx2 v[20:21], v[8:9], off offset:24
	v_and_b32_e32 v23, 0xffff0000, v27
	v_and_b32_e32 v22, 0xffff0000, v31
	s_waitcnt vmcnt(0)
	v_pk_mul_f32 v[24:25], v[20:21], v[22:23] op_sel:[0,1] op_sel_hi:[1,0]
	v_pk_mul_f32 v[20:21], v[20:21], v[22:23]
	v_sub_f32_e32 v24, v24, v25
	v_add_f32_e32 v20, v20, v21
	v_cvt_pk_bf16_f32 v21, v24, v193
	v_cvt_pk_bf16_f32 v20, v20, v193
	global_load_dwordx2 v[22:23], v[8:9], off offset:32
	v_lshlrev_b32_e32 v25, 16, v28
	v_lshlrev_b32_e32 v24, 16, v32
	s_waitcnt vmcnt(0)
	v_pk_mul_f32 v[26:27], v[22:23], v[24:25] op_sel:[0,1] op_sel_hi:[1,0]
	v_pk_mul_f32 v[22:23], v[22:23], v[24:25]
	v_sub_f32_e32 v26, v26, v27
	v_add_f32_e32 v22, v22, v23
	v_cvt_pk_bf16_f32 v23, v26, v193
	v_cvt_pk_bf16_f32 v22, v22, v193
	global_load_dwordx2 v[24:25], v[8:9], off offset:40
	v_and_b32_e32 v27, 0xffff0000, v28
	v_and_b32_e32 v26, 0xffff0000, v32
	s_waitcnt vmcnt(0)
	v_pk_mul_f32 v[30:31], v[24:25], v[26:27] op_sel:[0,1] op_sel_hi:[1,0]
	v_pk_mul_f32 v[24:25], v[24:25], v[26:27]
	v_sub_f32_e32 v28, v30, v31
	v_add_f32_e32 v24, v24, v25
	v_cvt_pk_bf16_f32 v25, v28, v193
	v_cvt_pk_bf16_f32 v24, v24, v193
	global_load_dwordx2 v[26:27], v[8:9], off offset:48
	v_lshlrev_b32_e32 v31, 16, v29
	v_lshlrev_b32_e32 v30, 16, v33
	v_and_b32_e32 v29, 0xffff0000, v29
	s_waitcnt vmcnt(0)
; __device__ __forceinline__ unsigned cvt_pk_bf16(float lo, float hi) { unsigned r; asm volatile("v_cvt_pk_bf16_f32 %0, %1, %2" : "=v"(r) : "v"(lo), "v"(hi)); return r; }
;     ...
;             const f32x2* rt = P.ropeM + (size_t)(qrow & (SEQ - 1)) * 32;
; #pragma unroll
;             for (int g = 0; g < 2; ++g) {
;                 bf16x8 x1 = qr[8 + g], x2 = qr[10 + g];
; #pragma unroll
;                 for (int e = 0; e < 8; ++e) { const f32x2 cs = rt[g * 16 + hi * 8 + e];
;                     const float a = bf2f((unsigned short)x1[e]), c = bf2f((unsigned short)x2[e]);
;                     const float ra = a * cs.x - c * cs.y, rc = c * cs.x + a * cs.y;
;                     x1[e] = (short)(cvt_pk_bf16(ra, 0.f) & 0xffffu); x2[e] = (short)(cvt_pk_bf16(rc, 0.f) & 0xffffu); }
;                 qr[8 + g] = x1; qr[10 + g] = x2;
	v_pk_mul_f32 v[34:35], v[26:27], v[30:31] op_sel:[0,1] op_sel_hi:[1,0]
	v_pk_mul_f32 v[26:27], v[26:27], v[30:31]
	v_sub_f32_e32 v28, v34, v35
	v_add_f32_e32 v26, v26, v27
	v_cvt_pk_bf16_f32 v27, v28, v193
	v_cvt_pk_bf16_f32 v26, v26, v193
	global_load_dwordx2 v[30:31], v[8:9], off offset:56
	v_and_b32_e32 v28, 0xffff0000, v33
	v_lshlrev_b32_e32 v35, 16, v0
	v_lshlrev_b32_e32 v34, 16, v4
	s_waitcnt vmcnt(0)
	v_pk_mul_f32 v[32:33], v[30:31], v[28:29] op_sel:[0,1] op_sel_hi:[1,0]
	v_pk_mul_f32 v[28:29], v[30:31], v[28:29]
	v_sub_f32_e32 v32, v32, v33
	v_add_f32_e32 v28, v28, v29
	v_cvt_pk_bf16_f32 v30, v32, v193
	v_cvt_pk_bf16_f32 v28, v28, v193
	global_load_dwordx2 v[32:33], v[8:9], off offset:128
	s_waitcnt vmcnt(0)
	v_pk_mul_f32 v[36:37], v[32:33], v[34:35] op_sel:[0,1] op_sel_hi:[1,0]
	v_pk_mul_f32 v[32:33], v[32:33], v[34:35]
	v_sub_f32_e32 v29, v36, v37
	v_add_f32_e32 v32, v32, v33
	v_cvt_pk_bf16_f32 v31, v29, v193
	v_cvt_pk_bf16_f32 v29, v32, v193
	global_load_dwordx2 v[32:33], v[8:9], off offset:136
	v_and_b32_e32 v35, 0xffff0000, v0
	v_and_b32_e32 v34, 0xffff0000, v4
	s_waitcnt vmcnt(0)
	v_pk_mul_f32 v[36:37], v[32:33], v[34:35] op_sel:[0,1] op_sel_hi:[1,0]
	v_pk_mul_f32 v[32:33], v[32:33], v[34:35]
	v_sub_f32_e32 v0, v36, v37
	v_add_f32_e32 v4, v32, v33
	v_cvt_pk_bf16_f32 v32, v0, v193
	v_cvt_pk_bf16_f32 v4, v4, v193
	global_load_dwordx2 v[34:35], v[8:9], off offset:144
	v_lshlrev_b32_e32 v37, 16, v1
	v_lshlrev_b32_e32 v36, 16, v5
	v_and_b32_e32 v1, 0xffff0000, v1
	s_waitcnt vmcnt(0)
	v_pk_mul_f32 v[38:39], v[34:35], v[36:37] op_sel:[0,1] op_sel_hi:[1,0]
	v_pk_mul_f32 v[34:35], v[34:35], v[36:37]
	v_sub_f32_e32 v0, v38, v39
	v_add_f32_e32 v33, v34, v35
	v_cvt_pk_bf16_f32 v34, v0, v193
	v_cvt_pk_bf16_f32 v33, v33, v193
	global_load_dwordx2 v[36:37], v[8:9], off offset:152
	v_and_b32_e32 v0, 0xffff0000, v5
	s_waitcnt vmcnt(0)
	v_pk_mul_f32 v[38:39], v[36:37], v[0:1] op_sel:[0,1] op_sel_hi:[1,0]
	v_pk_mul_f32 v[0:1], v[36:37], v[0:1]
	v_sub_f32_e32 v5, v38, v39
	v_add_f32_e32 v0, v0, v1
	v_cvt_pk_bf16_f32 v35, v5, v193
	v_cvt_pk_bf16_f32 v5, v0, v193
	global_load_dwordx2 v[0:1], v[8:9], off offset:160
	v_lshlrev_b32_e32 v37, 16, v2
	v_lshlrev_b32_e32 v36, 16, v6
	s_waitcnt vmcnt(0)
	v_pk_mul_f32 v[38:39], v[0:1], v[36:37] op_sel:[0,1] op_sel_hi:[1,0]
	v_pk_mul_f32 v[0:1], v[0:1], v[36:37]
	v_sub_f32_e32 v38, v38, v39
	v_add_f32_e32 v0, v0, v1
	v_cvt_pk_bf16_f32 v37, v38, v193
	v_cvt_pk_bf16_f32 v36, v0, v193
	global_load_dwordx2 v[0:1], v[8:9], off offset:168
	v_and_b32_e32 v39, 0xffff0000, v2
	v_and_b32_e32 v38, 0xffff0000, v6
	s_waitcnt vmcnt(0)
	v_pk_mul_f32 v[40:41], v[0:1], v[38:39] op_sel:[0,1] op_sel_hi:[1,0]
	v_pk_mul_f32 v[0:1], v[0:1], v[38:39]
	v_sub_f32_e32 v2, v40, v41
	v_add_f32_e32 v0, v0, v1
	v_cvt_pk_bf16_f32 v6, v2, v193
	v_cvt_pk_bf16_f32 v2, v0, v193
	global_load_dwordx2 v[0:1], v[8:9], off offset:176
	v_lshlrev_b32_e32 v39, 16, v3
	v_lshlrev_b32_e32 v38, 16, v7
	s_waitcnt vmcnt(0)
	v_pk_mul_f32 v[40:41], v[0:1], v[38:39] op_sel:[0,1] op_sel_hi:[1,0]
	v_pk_mul_f32 v[0:1], v[0:1], v[38:39]
	v_sub_f32_e32 v40, v40, v41
	v_add_f32_e32 v0, v0, v1
	v_cvt_pk_bf16_f32 v39, v40, v193
	v_cvt_pk_bf16_f32 v38, v0, v193
	global_load_dwordx2 v[0:1], v[8:9], off offset:184
	v_and_b32_e32 v9, 0xffff0000, v3
	v_and_b32_e32 v8, 0xffff0000, v7
	s_waitcnt vmcnt(0)
; #define VM_WAIT() asm volatile("s_waitcnt vmcnt(0)" ::: "memory")
;     ...
;         unsigned gsv[2], gsk[2], gsk2 = 0u;
; #pragma unroll
;         for (int i = 0; i < 2; ++i) { const int a = (i * 512 + tid) * 16;
;             { const int sub = a >> 9, within = a & 511; const int kk = (sub >> 2) * 8 + (within >> 6); const int k = (kk & ~0xC) | ((kk & 4) << 1) | ((kk & 8) >> 1);
;               const int c = (sub & 3) * 32 + ((within & 63) >> 1); gsv[i] = (unsigned)(k * ldv + c) * 2u; }
;             if constexpr (MODE == MODE_DIFF) { if (i == 0) { const int row = a >> 7, ch = ((a >> 4) & 7) ^ ((row >> 1) & 7); gsk[0] = (unsigned)(row * ldk + ch * 8) * 2u; } gsk[1] = 0u; }
;             else { const int row = a >> 8, ch = ((a >> 4) & 15) ^ (row & 15); gsk[i] = (unsigned)(row * ldk + ch * 8) * 2u; } }
;         if constexpr (MODE == MODE_MLA) { const int a = tid * 16, row = a >> 7, ch = ((a >> 4) & 7) ^ ((row >> 1) & 7); gsk2 = (unsigned)(row * UW + ch * 8) * 2u; }
;         const unsigned ldsw = (unsigned)__builtin_amdgcn_readfirstlane(wid) * 1024u;
;     ...
;         GLDS(0, 0); VM_WAIT(); __syncthreads();
	v_pk_mul_f32 v[40:41], v[0:1], v[8:9] op_sel:[0,1] op_sel_hi:[1,0]
	v_pk_mul_f32 v[0:1], v[0:1], v[8:9]
	v_sub_f32_e32 v3, v40, v41
	v_add_f32_e32 v0, v0, v1
	v_bfe_i32 v9, v11, 4, 24
	v_cvt_pk_bf16_f32 v8, v3, v193
	v_cvt_pk_bf16_f32 v7, v0, v193
	v_bfe_u32 v0, v11, 2, 2
	v_lshrrev_b32_e32 v1, 1, v11
	v_lshlrev_b32_e32 v3, 1, v11
	v_lshrrev_b32_e32 v41, 1, v9
	v_and_or_b32 v0, v1, 8, v0
	v_and_b32_e32 v1, 0xc0, v3
	v_and_b32_e32 v40, 0xffff0, v9
	v_and_b32_e32 v41, 4, v41
	v_and_or_b32 v1, v13, 48, v1
	v_or3_b32 v40, v40, v41, v0
	v_lshl_or_b32 v192, v40, 12, v1
	v_xor_b32_e32 v40, v9, v11
	v_lshlrev_b32_e32 v9, 12, v9
	v_lshlrev_b32_e32 v40, 4, v40
	v_and_or_b32 v146, v40, s87, v9
	v_add_u32_e32 v9, 0x2000, v13
	v_ashrrev_i32_e32 v9, 8, v9
	v_lshrrev_b32_e32 v41, 1, v9
	v_and_b32_e32 v40, 0xffff0, v9
	v_and_b32_e32 v41, 4, v41
	v_or3_b32 v0, v40, v41, v0
	v_lshl_add_u64 v[40:41], s[0:1], 0, v[192:193]
	v_lshl_or_b32 v148, v0, 12, v1
	v_lshl_add_u64 v[40:41], v[40:41], 0, s[36:37]
	global_load_lds_dwordx4 v[40:41], off
	v_lshl_add_u64 v[40:41], s[0:1], 0, v[148:149]
	v_xor_b32_e32 v0, v9, v11
	v_lshl_add_u64 v[40:41], v[40:41], 0, s[36:37]
	s_add_i32 m0, s29, 0x2000
	v_lshlrev_b32_e32 v1, 12, v9
	v_lshlrev_b32_e32 v0, 4, v0
	global_load_lds_dwordx4 v[40:41], off
	s_mov_b32 m0, s2
	v_and_or_b32 v150, v0, s87, v1
	global_load_lds_dwordx4 v146, s[0:1]
	s_add_i32 m0, s29, 0xe000
	v_lshlrev_b32_e32 v0, 10, v11
	global_load_lds_dwordx4 v150, s[0:1]
	s_lshl_b64 s[0:1], s[4:5], 13
	v_and_b32_e32 v0, 0xffffe000, v0
	v_xor_b32_e32 v1, v13, v11
	s_add_u32 s0, s14, s0
	v_and_or_b32 v0, v1, s3, v0
	s_addc_u32 s1, s15, s1
	s_add_i32 m0, s29, 0x10000
	v_mov_b32_e32 v1, v193
	global_load_lds_dwordx4 v0, s[0:1]
	v_lshl_add_u64 v[152:153], s[14:15], 0, v[0:1]
	v_bitop3_b32 v0, v155, v11, 15 bitop3:0x78
	v_lshlrev_b32_e32 v9, 3, v11
	v_lshlrev_b32_e32 v158, 4, v0
	v_and_b32_e32 v0, 0xf0, v13
	v_bitop3_b32 v159, v144, v0, 32 bitop3:0x36
	v_bitop3_b32 v160, v144, v0, 64 bitop3:0x36
	v_bitop3_b32 v161, v144, v0, s60 bitop3:0x36
	v_bitop3_b32 v162, v144, v0, s59 bitop3:0x36
	v_bitop3_b32 v164, v144, v0, s61 bitop3:0x36
	v_bitop3_b32 v165, v144, v0, s58 bitop3:0x36
	v_bitop3_b32 v166, v144, v0, s62 bitop3:0x36
	v_and_b32_e32 v0, 0x70, v9
	v_bitop3_b32 v169, v144, v0, 32 bitop3:0x36
	v_bitop3_b32 v170, v144, v0, 64 bitop3:0x36
	v_bitop3_b32 v171, v144, v0, s60 bitop3:0x36
	v_and_b32_e32 v0, 0x118, v9
	s_mov_b32 s0, 0x5040100
	s_waitcnt vmcnt(0)
	v_perm_b32 v128, v17, v15, s0
	v_perm_b32 v136, v16, v14, s0
	v_and_or_b32 v0, v3, 32, v0
	v_mov_b32_e32 v14, v193
	v_mov_b32_e32 v15, v193
	v_bitop3_b32 v168, v144, v9, s3 bitop3:0x78
	v_cmp_gt_u32_e64 s[2:3], 32, v10
	v_perm_b32 v129, v21, v19, s0
	v_perm_b32 v130, v25, v23, s0
	v_perm_b32 v131, v30, v27, s0
	v_perm_b32 v132, v32, v31, s0
	v_perm_b32 v133, v35, v34, s0
	v_perm_b32 v134, v6, v37, s0
	v_perm_b32 v135, v8, v39, s0
	v_perm_b32 v137, v20, v18, s0
	v_perm_b32 v138, v24, v22, s0
	v_perm_b32 v139, v28, v26, s0
	v_perm_b32 v140, v4, v29, s0
	v_perm_b32 v141, v5, v33, s0
	v_perm_b32 v142, v2, v36, s0
	v_perm_b32 v143, v7, v38, s0
	v_add3_u32 v172, v12, 0, v0
	v_mov_b32_e32 v0, v193
	v_mov_b32_e32 v2, v193
	v_mov_b32_e32 v3, v193
	v_mov_b32_e32 v4, v193
	v_mov_b32_e32 v5, v193
	v_mov_b32_e32 v6, v193
	v_mov_b32_e32 v7, v193
	v_mov_b32_e32 v8, v193
	v_mov_b32_e32 v9, v193
	v_mov_b32_e32 v10, v193
	v_mov_b32_e32 v11, v193
	v_mov_b32_e32 v12, v193
	v_mov_b32_e32 v13, v193
	v_mov_b64_e32 v[30:31], v[14:15]
	v_mov_b64_e32 v[46:47], v[14:15]
	v_mov_b64_e32 v[62:63], v[14:15]
	s_or_b32 s16, s4, 64
	v_mov_b64_e32 v[28:29], v[12:13]
	v_mov_b64_e32 v[26:27], v[10:11]
	v_mov_b64_e32 v[24:25], v[8:9]
	v_mov_b64_e32 v[22:23], v[6:7]
	v_mov_b64_e32 v[20:21], v[4:5]
	v_mov_b64_e32 v[18:19], v[2:3]
	v_mov_b64_e32 v[16:17], v[0:1]
	v_mov_b64_e32 v[44:45], v[12:13]
	v_mov_b64_e32 v[42:43], v[10:11]
	v_mov_b64_e32 v[40:41], v[8:9]
	v_mov_b64_e32 v[38:39], v[6:7]
	v_mov_b64_e32 v[36:37], v[4:5]
	v_mov_b64_e32 v[34:35], v[2:3]
	v_mov_b64_e32 v[32:33], v[0:1]
	v_mov_b64_e32 v[60:61], v[12:13]
	v_mov_b64_e32 v[58:59], v[10:11]
	v_mov_b64_e32 v[56:57], v[8:9]
	v_mov_b64_e32 v[54:55], v[6:7]
	v_mov_b64_e32 v[52:53], v[4:5]
	v_mov_b64_e32 v[50:51], v[2:3]
	v_mov_b64_e32 v[48:49], v[0:1]
	s_waitcnt vmcnt(0) lgkmcnt(0)
	s_barrier
	s_and_b32 s30, s28, 1
	s_cmp_eq_u32 s28, 63
	s_cbranch_scc1 .LBB0_788
	s_branch .LBB0_787

; #define LAS __attribute__((address_space(3)))
; __device__ __forceinline__ float clamp8(float x) { return __builtin_amdgcn_fmed3f(x, -448.f, 448.f); }
; #define SBAR() __builtin_amdgcn_sched_barrier(0)
; #define NAMASK(pa_, pb_, t) do { if constexpr (MODE == MODE_NA) na_bias_mask(pa_, pb_, rpbL, kr_lo + (t), rq, qc, hi); } while (0)
;     ...
;         for (int t = 0; t < NT; ++t) {
;             const int bf = t & 1;
;             if (t + 1 < NT) GLDS(t + 1, bf ^ 1);
;             SBAR();
;             bool act = true;
;             if constexpr (MODE == MODE_NA) { const int kr = kr_lo + t, r0w = min(max(rq - 4, 0), 56); act = (kr >= r0w) && (kr < r0w + 8); }
;             if (act) {
;             qkt<MODE>(p0, p1, K_lds + bf * SHM_K, qr, r32, hi); NAMASK(p0, p1, t);
; __device__ __forceinline__ void cvt_finish(const CvtDesc& d, const float (&t)[64], LAS float* scr, int lane) {
;     ...
;     if (d.f8) {
; #pragma unroll
;         for (int j = 0; j < 8; ++j) { const int n = (lane >> 3) + 8 * j; const LAS float* s = scr + (8 * c) * 65 + n;
;             int a = __builtin_amdgcn_cvt_pk_fp8_f32(clamp8(s[0 * 65] * W8_SCALE), clamp8(s[1 * 65] * W8_SCALE), 0, false); a = __builtin_amdgcn_cvt_pk_fp8_f32(clamp8(s[2 * 65] * W8_SCALE), clamp8(s[3 * 65] * W8_SCALE), a, true);
;             int b = __builtin_amdgcn_cvt_pk_fp8_f32(clamp8(s[4 * 65] * W8_SCALE), clamp8(s[5 * 65] * W8_SCALE), 0, false); b = __builtin_amdgcn_cvt_pk_fp8_f32(clamp8(s[6 * 65] * W8_SCALE), clamp8(s[7 * 65] * W8_SCALE), b, true);
;             __builtin_nontemporal_store((u32x2){(unsigned)a, (unsigned)b}, (u32x2*)(d.dst + (size_t)n * d.dKB + 8 * c)); }
.LBB0_788:
	s_add_u32 s52, s52, 33
	s_cmp_ge_u32 s52, 63
	s_cselect_b32 s50, 1, 0
	s_cbranch_scc0 .Lilc_n_m
	s_sub_u32 s52, s52, 63
	s_mov_b32 s46, s51
	s_add_u32 s51, s51, 1
	s_lshl_b32 s49, s46, 2
	s_add_u32 s49, s49, s54
	s_cmp_lt_u32 s49, 0xc3
	s_cselect_b32 s50, 1, 0
	s_cbranch_scc0 .Lilc_n_m
	s_lshr_b32 s55, s46, 4
	s_and_b32 s57, s49, 63
	s_lshl_b32 s101, s56, 6
	s_add_u32 s101, s101, s57
	s_cmp_eq_u32 s55, 3
	s_cselect_b32 s55, s54, s55
	s_cselect_b32 s100, 3, 0
	s_cselect_b32 s101, s56, s101
	s_cselect_b32 s57, 64, s57
	s_add_u32 s100, s100, s55
	s_lshl_b32 s100, s100, 3
	s_add_u32 s100, s100, 0xa0
	s_load_dwordx2 s[44:45], s[6:7], s100
.Lilc_n_m:
	s_cmp_eq_u32 s42, 0
	s_cbranch_scc1 .Lilc_np_m
	s_cmp_eq_u32 s53, 0
	s_cbranch_scc1 .Lilc_p_m
	s_cmp_eq_u32 s50, 0
	s_cbranch_scc1 .Lilc_np_m
	s_waitcnt vmcnt(0)
.Lilc_p_m:
	s_mov_b32 s53, 4
	v_mul_f32_e32 v232, 0x42800000, v232
	v_mul_f32_e32 v233, 0x42800000, v233
	v_mul_f32_e32 v234, 0x42800000, v234
	v_mul_f32_e32 v235, 0x42800000, v235
	v_mul_f32_e32 v236, 0x42800000, v236
	v_mul_f32_e32 v237, 0x42800000, v237
	v_mul_f32_e32 v238, 0x42800000, v238
	v_mul_f32_e32 v239, 0x42800000, v239
	v_mul_f32_e32 v240, 0x42800000, v240
	v_mul_f32_e32 v241, 0x42800000, v241
	v_mul_f32_e32 v242, 0x42800000, v242
	v_mul_f32_e32 v243, 0x42800000, v243
	v_mul_f32_e32 v244, 0x42800000, v244
	v_mul_f32_e32 v245, 0x42800000, v245
	v_mul_f32_e32 v246, 0x42800000, v246
	v_mul_f32_e32 v247, 0x42800000, v247
	v_mul_f32_e32 v248, 0x42800000, v248
	v_mul_f32_e32 v249, 0x42800000, v249
	v_mul_f32_e32 v250, 0x42800000, v250
	v_mul_f32_e32 v251, 0x42800000, v251
	v_mul_f32_e32 v206, 0x42800000, v206
	v_mul_f32_e32 v207, 0x42800000, v207
	v_mul_f32_e32 v208, 0x42800000, v208
	v_mul_f32_e32 v209, 0x42800000, v209
	v_mul_f32_e32 v210, 0x42800000, v210
	v_mul_f32_e32 v211, 0x42800000, v211
	v_mul_f32_e32 v212, 0x42800000, v212
	v_mul_f32_e32 v213, 0x42800000, v213
	v_mul_f32_e32 v214, 0x42800000, v214
	v_mul_f32_e32 v215, 0x42800000, v215
	v_mul_f32_e32 v216, 0x42800000, v216
	v_mul_f32_e32 v217, 0x42800000, v217
	v_med3_f32 v232, v232, s93, v224
	v_med3_f32 v233, v233, s93, v224
	v_med3_f32 v234, v234, s93, v224
	v_med3_f32 v235, v235, s93, v224
	v_med3_f32 v236, v236, s93, v224
	v_med3_f32 v237, v237, s93, v224
	v_med3_f32 v238, v238, s93, v224
	v_med3_f32 v239, v239, s93, v224
	v_med3_f32 v240, v240, s93, v224
	v_med3_f32 v241, v241, s93, v224
	v_med3_f32 v242, v242, s93, v224
	v_med3_f32 v243, v243, s93, v224
	v_med3_f32 v244, v244, s93, v224
	v_med3_f32 v245, v245, s93, v224
	v_med3_f32 v246, v246, s93, v224
	v_med3_f32 v247, v247, s93, v224
	v_med3_f32 v248, v248, s93, v224
	v_med3_f32 v249, v249, s93, v224
	v_med3_f32 v250, v250, s93, v224
	v_med3_f32 v251, v251, s93, v224
	v_med3_f32 v206, v206, s93, v224
	v_med3_f32 v207, v207, s93, v224
	v_med3_f32 v208, v208, s93, v224
	v_med3_f32 v209, v209, s93, v224
	v_med3_f32 v210, v210, s93, v224
	v_med3_f32 v211, v211, s93, v224
	v_med3_f32 v212, v212, s93, v224
	v_med3_f32 v213, v213, s93, v224
	v_med3_f32 v214, v214, s93, v224
	v_med3_f32 v215, v215, s93, v224
	v_med3_f32 v216, v216, s93, v224
	v_med3_f32 v217, v217, s93, v224
	v_lshlrev_b32_e32 v230, 3, v226
	v_lshl_add_u32 v225, v229, s42, v230
	v_cvt_pk_fp8_f32 v252, v232, v236
	v_cvt_pk_fp8_f32 v253, v248, v206
	v_cvt_pk_fp8_f32 v252, v240, v244 op_sel:[0,0,1]
	v_cvt_pk_fp8_f32 v253, v210, v214 op_sel:[0,0,1]
	s_nop 0
	global_store_dwordx2 v225, v[252:253], s[40:41]
	v_add_u32_e32 v225, s43, v225
	v_cvt_pk_fp8_f32 v252, v233, v237
	v_cvt_pk_fp8_f32 v253, v249, v207
	v_cvt_pk_fp8_f32 v252, v241, v245 op_sel:[0,0,1]
	v_cvt_pk_fp8_f32 v253, v211, v215 op_sel:[0,0,1]
	s_nop 0
	global_store_dwordx2 v225, v[252:253], s[40:41]
	v_add_u32_e32 v225, s43, v225
	v_cvt_pk_fp8_f32 v252, v234, v238
	v_cvt_pk_fp8_f32 v253, v250, v208
	v_cvt_pk_fp8_f32 v252, v242, v246 op_sel:[0,0,1]
	v_cvt_pk_fp8_f32 v253, v212, v216 op_sel:[0,0,1]
	s_nop 0
	global_store_dwordx2 v225, v[252:253], s[40:41]
	v_add_u32_e32 v225, s43, v225
	v_cvt_pk_fp8_f32 v252, v235, v239
	v_cvt_pk_fp8_f32 v253, v251, v209
	v_cvt_pk_fp8_f32 v252, v243, v247 op_sel:[0,0,1]
	v_cvt_pk_fp8_f32 v253, v213, v217 op_sel:[0,0,1]
	s_nop 0
	global_store_dwordx2 v225, v[252:253], s[40:41]
	s_mov_b32 s42, 0
	s_branch .Lilc_i_m

;     __device__ __forceinline__ const float* in(int i) const { return *(const float* const __attribute__((address_space(4)))*)(p + 8 * i); }
;     __device__ __forceinline__ unsigned char* ws() const { return *(unsigned char* const __attribute__((address_space(4)))*)(p + 232); }
; __device__ __forceinline__ CvtDesc conv_expert_desc(const KA& a, unsigned char* ws, int q) {
;     const int l = q / Q_PER_L; int r = q - l * Q_PER_L;
;     unsigned char* wl = ws + WS_W + (size_t)l * W_LSTRIDE;
;     CvtDesc d; d.f8 = (MOE_FP8_LAST && (MOE_FP8_GU_ALL || l == NLAYER - 1)) ? 1 : 0;
;     if (MOE_FP8_LAST && MOE_FP8_DOWN_ALL && r >= 2 * Q_IG) d.f8 = 1;
;     const int eb = d.f8 ? 1 : 2;
;     if (r < 2 * Q_IG) { const int up = r >= Q_IG; if (up) r -= Q_IG; const int e = r >> 8, rr = r & 255, kb = rr >> 3, nb = rr & 7, n0 = nb * 64;
;         const float* src = e < 64 ? a.in(up ? 21 : 20) + ((size_t)l * 64 + e) * DM * FFE : a.in(up ? 24 : 23) + (size_t)l * DM * FFE;
;         d.src = src + (size_t)(kb * 64) * FFE + n0; d.N = FFE; d.dKB = DM * eb;
;         d.dst = wl + W_GU + ((size_t)e * 1024 * DM + (size_t)((n0 >> 7) * 256 + up * 128 + (n0 & 127)) * DM + kb * 64) * eb;
;     } else { r -= 2 * Q_IG; const int e = r >> 8, rr = r & 255, kb = rr >> 5, nb = rr & 31;
;         const float* src = e < 64 ? a.in(22) + ((size_t)l * 64 + e) * FFE * DM : a.in(25) + (size_t)l * FFE * DM;
;         d.src = src + (size_t)(kb * 64) * DM + nb * 64; d.N = DM; d.dKB = FFE * eb;
;         d.dst = wl + W_D + ((size_t)e * DM * FFE + (size_t)(nb * 64) * FFE + kb * 64) * eb; }
.Lilc_i_m:
	s_cmp_eq_u32 s50, 0
	s_cbranch_scc1 .Lilc_d_m
	s_waitcnt lgkmcnt(0)
	s_lshr_b32 s49, s101, 10
	s_lshl_b32 s101, s101, 22
	s_add_u32 s44, s44, s101
	s_addc_u32 s45, s45, s49
	s_cmp_eq_u32 s55, 2
	s_cbranch_scc1 .Lilc_dn_m
	s_lshr_b32 s49, s39, 4
	s_and_b32 s46, s39, 15
	s_lshl_b32 s100, s49, 17
	s_lshl_b32 s101, s46, 7
	s_add_u32 s100, s100, s101
	s_add_u32 s44, s44, s100
	s_addc_u32 s45, s45, 0
	s_lshr_b32 s100, s46, 2
	s_lshl_b32 s100, s100, 8
	s_lshl_b32 s101, s55, 7
	s_add_u32 s100, s100, s101
	s_and_b32 s101, s46, 3
	s_lshl_b32 s101, s101, 5
	s_add_u32 s100, s100, s101
	s_lshl_b32 s100, s100, 11
	s_lshl_b32 s101, s49, 6
	s_add_u32 s100, s100, s101
	s_lshl_b32 s101, s57, 21
	s_add_u32 s100, s100, s101
	s_add_u32 s100, s100, 0x34000000
	s_mul_i32 s101, s56, 0x1a800000
	s_add_u32 s100, s100, s101
	s_add_u32 s40, s8, s100
	s_addc_u32 s41, s9, 0
	s_mov_b32 s42, 13
	s_movk_i32 s43, 0x800
	s_movk_i32 s47, 0x800
	s_mov_b32 s48, 14
	s_branch .Lilc_is_m

; #define SBAR() __builtin_amdgcn_sched_barrier(0)
; template <int MODE>
; __device__ __forceinline__ void partialSM(f32x16& p0, f32x16& p1, float& m_reg, float& mn, float& alpha) {
;     ...
;     const float mnC = -mn * C;
; #pragma unroll
;     for (int r = 0; r < 16; ++r) p0[r] = fmaf(p0[r], C, mnC);
; #pragma unroll
;     for (int r = 0; r < 16; ++r) p1[r] = fmaf(p1[r], C, mnC);
; #pragma unroll
;     for (int r = 0; r < 16; ++r) p0[r] = __builtin_amdgcn_exp2f(p0[r]);
; }
; __device__ __forceinline__ void finishSM(f32x16& p0, f32x16& p1, float alpha, float& l_reg, bf16x8& pa0, bf16x8& pa1, bf16x8& pa2, bf16x8& pa3) {
; #pragma unroll
;     for (int r = 0; r < 16; ++r) p1[r] = __builtin_amdgcn_exp2f(p1[r]);
;     float ps = 0;
; #pragma unroll
;     for (int r = 0; r < 16; ++r) ps += p0[r];
; #pragma unroll
;     for (int r = 0; r < 16; ++r) ps += p1[r];
;     { auto rr = __builtin_amdgcn_permlane32_swap(__float_as_uint(ps), __float_as_uint(ps), false, false);
;       ps = __uint_as_float(rr[0]) + __uint_as_float(rr[1]); }
;     l_reg = l_reg * alpha + ps;
;     ...
;     PK4(p0, 0, pa0); PK4(p0, 8, pa1); PK4(p1, 0, pa2); PK4(p1, 8, pa3);
;     ...
; }
; template <int D0> __device__ __forceinline__ void pv_one(f32x16& od, int vb, bf16x8 pa0, bf16x8 pa1, bf16x8 pa2, bf16x8 pa3) {
;     const s16x4 l0 = tr_read<v_rd_off(D0, 0, 0)>(vb), h0 = tr_read<v_rd_off(D0, 0, 1)>(vb), l1 = tr_read<v_rd_off(D0, 1, 0)>(vb), h1 = tr_read<v_rd_off(D0, 1, 1)>(vb);
;     const s16x4 l2 = tr_read<v_rd_off(D0, 2, 0)>(vb), h2 = tr_read<v_rd_off(D0, 2, 1)>(vb), l3 = tr_read<v_rd_off(D0, 3, 0)>(vb), h3 = tr_read<v_rd_off(D0, 3, 1)>(vb);
;     asm volatile("s_waitcnt lgkmcnt(0)" ::: "memory"); SBAR();
;     ...
;     od = __builtin_amdgcn_mfma_f32_32x32x16_bf16(pa0, PK(l0, h0), od, 0, 0, 0);
;     od = __builtin_amdgcn_mfma_f32_32x32x16_bf16(pa1, PK(l1, h1), od, 0, 0, 0);
;     od = __builtin_amdgcn_mfma_f32_32x32x16_bf16(pa2, PK(l2, h2), od, 0, 0, 0);
;     od = __builtin_amdgcn_mfma_f32_32x32x16_bf16(pa3, PK(l3, h3), od, 0, 0, 0);
;     ...
; }
; __device__ __forceinline__ void pv_d0(f32x16* o, int vb, bf16x8 pa0, bf16x8 pa1, bf16x8 pa2, bf16x8 pa3) {
;     pv_one<0>(o[0], vb, pa0, pa1, pa2, pa3); pv_one<1>(o[1], vb, pa0, pa1, pa2, pa3); pv_one<2>(o[2], vb, pa0, pa1, pa2, pa3); pv_one<3>(o[3], vb, pa0, pa1, pa2, pa3);
; }
.LBB0_792:
	v_cndmask_b32_e64 v173, v176, v173, s[4:5]
	v_mul_f32_e32 v176, 0xbdd53b94, v173
	v_fmamk_f32 v80, v80, 0x3dd53b94, v176
	v_fmamk_f32 v81, v81, 0x3dd53b94, v176
	v_fmamk_f32 v82, v82, 0x3dd53b94, v176
	v_fmamk_f32 v83, v83, 0x3dd53b94, v176
	v_fmamk_f32 v84, v84, 0x3dd53b94, v176
	v_fmamk_f32 v85, v85, 0x3dd53b94, v176
	v_fmamk_f32 v86, v86, 0x3dd53b94, v176
	v_fmamk_f32 v87, v87, 0x3dd53b94, v176
	v_fmamk_f32 v88, v88, 0x3dd53b94, v176
	v_fmamk_f32 v89, v89, 0x3dd53b94, v176
	v_fmamk_f32 v90, v90, 0x3dd53b94, v176
	v_fmamk_f32 v91, v91, 0x3dd53b94, v176
	v_fmamk_f32 v92, v92, 0x3dd53b94, v176
	v_fmamk_f32 v93, v93, 0x3dd53b94, v176
	v_fmamk_f32 v94, v94, 0x3dd53b94, v176
	v_fmamk_f32 v95, v95, 0x3dd53b94, v176
	v_fmamk_f32 v64, v64, 0x3dd53b94, v176
	v_fmamk_f32 v65, v65, 0x3dd53b94, v176
	v_fmamk_f32 v66, v66, 0x3dd53b94, v176
	v_fmamk_f32 v67, v67, 0x3dd53b94, v176
	v_fmamk_f32 v68, v68, 0x3dd53b94, v176
	v_fmamk_f32 v69, v69, 0x3dd53b94, v176
	v_fmamk_f32 v70, v70, 0x3dd53b94, v176
	v_fmamk_f32 v71, v71, 0x3dd53b94, v176
	v_fmamk_f32 v72, v72, 0x3dd53b94, v176
	v_fmamk_f32 v73, v73, 0x3dd53b94, v176
	v_fmamk_f32 v74, v74, 0x3dd53b94, v176
	v_fmamk_f32 v75, v75, 0x3dd53b94, v176
	v_fmamk_f32 v76, v76, 0x3dd53b94, v176
	v_fmamk_f32 v77, v77, 0x3dd53b94, v176
	v_fmamk_f32 v78, v78, 0x3dd53b94, v176
	v_fmac_f32_e32 v176, 0x3dd53b94, v79
	v_exp_f32_e32 v79, v80
	v_exp_f32_e32 v80, v81
	v_exp_f32_e32 v81, v82
	v_exp_f32_e32 v82, v83
	v_exp_f32_e32 v83, v84
	v_exp_f32_e32 v84, v85
	v_exp_f32_e32 v85, v86
	v_exp_f32_e32 v86, v87
	v_exp_f32_e32 v87, v88
	v_exp_f32_e32 v88, v89
	v_exp_f32_e32 v89, v90
	v_exp_f32_e32 v90, v91
	v_exp_f32_e32 v91, v92
	v_exp_f32_e32 v92, v93
	v_exp_f32_e32 v93, v94
	v_exp_f32_e32 v94, v95
	v_exp_f32_e32 v95, v64
	v_add_f32_e32 v64, 0, v79
	v_add_f32_e32 v64, v80, v64
	v_add_f32_e32 v64, v81, v64
	v_add_f32_e32 v64, v82, v64
	v_add_f32_e32 v64, v83, v64
	v_add_f32_e32 v64, v84, v64
	v_add_f32_e32 v64, v85, v64
	v_add_f32_e32 v64, v86, v64
	v_add_f32_e32 v64, v87, v64
	v_add_f32_e32 v64, v88, v64
	v_add_f32_e32 v64, v89, v64
	v_add_f32_e32 v64, v90, v64
	v_add_f32_e32 v64, v91, v64
	v_exp_f32_e32 v65, v65
	v_add_f32_e32 v64, v92, v64
	v_exp_f32_e32 v177, v66
	v_add_f32_e32 v64, v93, v64
	v_exp_f32_e32 v178, v67
	v_add_f32_e32 v64, v94, v64
	v_exp_f32_e32 v179, v68
	v_add_f32_e32 v64, v95, v64
	v_exp_f32_e32 v180, v69
	v_add_f32_e32 v64, v65, v64
	v_exp_f32_e32 v181, v70
	v_add_f32_e32 v64, v177, v64
	v_exp_f32_e32 v182, v71
	v_add_f32_e32 v64, v178, v64
	v_exp_f32_e32 v183, v72
	v_add_f32_e32 v64, v179, v64
	v_exp_f32_e32 v184, v73
	v_add_f32_e32 v64, v180, v64
	v_exp_f32_e32 v185, v74
	v_add_f32_e32 v64, v181, v64
	v_exp_f32_e32 v186, v75
	v_add_f32_e32 v64, v182, v64
	v_exp_f32_e32 v187, v76
	v_add_f32_e32 v64, v183, v64
	v_exp_f32_e32 v188, v77
	v_add_f32_e32 v64, v184, v64
	v_exp_f32_e32 v189, v78
	v_add_f32_e32 v64, v185, v64
	v_exp_f32_e32 v176, v176
	v_add_f32_e32 v64, v186, v64
	v_add_f32_e32 v64, v187, v64
	v_add_f32_e32 v64, v188, v64
	v_add_f32_e32 v64, v189, v64
	v_add_f32_e32 v64, v176, v64
	v_mov_b32_e32 v66, v64
	s_nop 1
	v_permlane32_swap_b32_e32 v64, v66
	v_add_f32_e32 v64, v64, v66
	s_add_i32 s28, s28, 1
	v_fmac_f32_e32 v64, v174, v175
	v_cvt_pk_bf16_f32 v66, v79, v80
	v_cvt_pk_bf16_f32 v67, v81, v82
	v_cvt_pk_bf16_f32 v68, v83, v84
	v_cvt_pk_bf16_f32 v69, v85, v86
	v_cvt_pk_bf16_f32 v70, v87, v88
	v_cvt_pk_bf16_f32 v71, v89, v90
	v_cvt_pk_bf16_f32 v72, v91, v92
	v_cvt_pk_bf16_f32 v73, v93, v94
	v_cvt_pk_bf16_f32 v74, v95, v65
	v_cvt_pk_bf16_f32 v75, v177, v178
	v_cvt_pk_bf16_f32 v76, v179, v180
	v_cvt_pk_bf16_f32 v77, v181, v182
	v_cvt_pk_bf16_f32 v78, v183, v184
	v_cvt_pk_bf16_f32 v79, v185, v186
	v_cvt_pk_bf16_f32 v80, v187, v188
	v_cvt_pk_bf16_f32 v81, v189, v176
	s_nop 0
	v_permlane32_swap_b32_e32 v66, v68
	v_permlane32_swap_b32_e32 v67, v69
	v_permlane32_swap_b32_e32 v70, v72
	v_permlane32_swap_b32_e32 v71, v73
	v_permlane32_swap_b32_e32 v74, v76
	v_permlane32_swap_b32_e32 v75, v77
	v_permlane32_swap_b32_e32 v78, v80
	v_permlane32_swap_b32_e32 v79, v81
	v_lshl_add_u32 v65, s30, 14, v172
	ds_read_b64_tr_b16 v[82:83], v65 offset:0
	ds_read_b64_tr_b16 v[84:85], v65 offset:0x800
	ds_read_b64_tr_b16 v[86:87], v65 offset:0x1000
	ds_read_b64_tr_b16 v[88:89], v65 offset:0x1800
	ds_read_b64_tr_b16 v[90:91], v65 offset:0x2000
	ds_read_b64_tr_b16 v[92:93], v65 offset:0x2800
	ds_read_b64_tr_b16 v[174:175], v65 offset:0x3000
	ds_read_b64_tr_b16 v[176:177], v65 offset:0x3800
	s_waitcnt lgkmcnt(0)
	s_nop 0
	v_mfma_f32_32x32x16_bf16 v[0:15], v[66:69], v[82:85], v[0:15]
	ds_read_b64_tr_b16 v[82:83], v65 offset:0x200
	ds_read_b64_tr_b16 v[84:85], v65 offset:0xa00
	v_mfma_f32_32x32x16_bf16 v[0:15], v[70:73], v[86:89], v[0:15]
	ds_read_b64_tr_b16 v[86:87], v65 offset:0x1200
	ds_read_b64_tr_b16 v[88:89], v65 offset:0x1a00
	v_mfma_f32_32x32x16_bf16 v[0:15], v[74:77], v[90:93], v[0:15]
	ds_read_b64_tr_b16 v[90:91], v65 offset:0x2200
	ds_read_b64_tr_b16 v[92:93], v65 offset:0x2a00
	v_mfma_f32_32x32x16_bf16 v[0:15], v[78:81], v[174:177], v[0:15]
	ds_read_b64_tr_b16 v[174:175], v65 offset:0x3200
	ds_read_b64_tr_b16 v[176:177], v65 offset:0x3a00
	s_waitcnt lgkmcnt(0)
	v_mfma_f32_32x32x16_bf16 v[16:31], v[66:69], v[82:85], v[16:31]
	ds_read_b64_tr_b16 v[82:83], v65 offset:0x400
	ds_read_b64_tr_b16 v[84:85], v65 offset:0xc00
	v_mfma_f32_32x32x16_bf16 v[16:31], v[70:73], v[86:89], v[16:31]
	ds_read_b64_tr_b16 v[86:87], v65 offset:0x1400
	ds_read_b64_tr_b16 v[88:89], v65 offset:0x1c00
	v_mfma_f32_32x32x16_bf16 v[16:31], v[74:77], v[90:93], v[16:31]
	ds_read_b64_tr_b16 v[90:91], v65 offset:0x2400
	ds_read_b64_tr_b16 v[92:93], v65 offset:0x2c00
	v_mfma_f32_32x32x16_bf16 v[16:31], v[78:81], v[174:177], v[16:31]
	ds_read_b64_tr_b16 v[174:175], v65 offset:0x3400
	ds_read_b64_tr_b16 v[176:177], v65 offset:0x3c00
	s_waitcnt lgkmcnt(0)
	v_mfma_f32_32x32x16_bf16 v[32:47], v[66:69], v[82:85], v[32:47]
	ds_read_b64_tr_b16 v[82:83], v65 offset:0x600
	ds_read_b64_tr_b16 v[84:85], v65 offset:0xe00
	v_mfma_f32_32x32x16_bf16 v[32:47], v[70:73], v[86:89], v[32:47]
	ds_read_b64_tr_b16 v[86:87], v65 offset:0x1600
	ds_read_b64_tr_b16 v[88:89], v65 offset:0x1e00
	v_mfma_f32_32x32x16_bf16 v[32:47], v[74:77], v[90:93], v[32:47]
	ds_read_b64_tr_b16 v[90:91], v65 offset:0x2600
	ds_read_b64_tr_b16 v[92:93], v65 offset:0x2e00
	v_mfma_f32_32x32x16_bf16 v[32:47], v[78:81], v[174:177], v[32:47]
	ds_read_b64_tr_b16 v[174:175], v65 offset:0x3600
	ds_read_b64_tr_b16 v[176:177], v65 offset:0x3e00
	s_waitcnt lgkmcnt(0)
	v_mfma_f32_32x32x16_bf16 v[48:63], v[66:69], v[82:85], v[48:63]
	s_add_i32 s16, s16, 64
	s_cmp_eq_u32 s53, 12
	s_cbranch_scc1 .Lilc_w12_m
	s_cmp_eq_u32 s53, 8
	s_cbranch_scc1 .Lilc_w8_m
	s_waitcnt vmcnt(0)
	s_branch .Lilc_wd_m

; #define LAS __attribute__((address_space(3)))
; __device__ __forceinline__ float clamp8(float x) { return __builtin_amdgcn_fmed3f(x, -448.f, 448.f); }
; #define VM_WAIT() asm volatile("s_waitcnt vmcnt(0)" ::: "memory")
;     ...
;             VM_WAIT();
;             __syncthreads();
;         }
; __device__ __forceinline__ void cvt_finish(const CvtDesc& d, const float (&t)[64], LAS float* scr, int lane) {
;     ...
;     if (d.f8) {
; #pragma unroll
;         for (int j = 0; j < 8; ++j) { const int n = (lane >> 3) + 8 * j; const LAS float* s = scr + (8 * c) * 65 + n;
;             int a = __builtin_amdgcn_cvt_pk_fp8_f32(clamp8(s[0 * 65] * W8_SCALE), clamp8(s[1 * 65] * W8_SCALE), 0, false); a = __builtin_amdgcn_cvt_pk_fp8_f32(clamp8(s[2 * 65] * W8_SCALE), clamp8(s[3 * 65] * W8_SCALE), a, true);
;             int b = __builtin_amdgcn_cvt_pk_fp8_f32(clamp8(s[4 * 65] * W8_SCALE), clamp8(s[5 * 65] * W8_SCALE), 0, false); b = __builtin_amdgcn_cvt_pk_fp8_f32(clamp8(s[6 * 65] * W8_SCALE), clamp8(s[7 * 65] * W8_SCALE), b, true);
;             __builtin_nontemporal_store((u32x2){(unsigned)a, (unsigned)b}, (u32x2*)(d.dst + (size_t)n * d.dKB + 8 * c)); }
.Lilc_wd_m:
	s_cmp_eq_u32 s28, 64
	s_barrier
	v_mfma_f32_32x32x16_bf16 v[48:63], v[70:73], v[86:89], v[48:63]
	v_mfma_f32_32x32x16_bf16 v[48:63], v[74:77], v[90:93], v[48:63]
	v_mfma_f32_32x32x16_bf16 v[48:63], v[78:81], v[174:177], v[48:63]
	s_cbranch_scc0 .LBB0_786
	s_cmp_eq_u32 s42, 0
	s_cbranch_scc1 .Lilc_fd_m
	s_waitcnt vmcnt(0)
	v_mul_f32_e32 v232, 0x42800000, v232
	v_mul_f32_e32 v233, 0x42800000, v233
	v_mul_f32_e32 v234, 0x42800000, v234
	v_mul_f32_e32 v235, 0x42800000, v235
	v_mul_f32_e32 v236, 0x42800000, v236
	v_mul_f32_e32 v237, 0x42800000, v237
	v_mul_f32_e32 v238, 0x42800000, v238
	v_mul_f32_e32 v239, 0x42800000, v239
	v_mul_f32_e32 v240, 0x42800000, v240
	v_mul_f32_e32 v241, 0x42800000, v241
	v_mul_f32_e32 v242, 0x42800000, v242
	v_mul_f32_e32 v243, 0x42800000, v243
	v_mul_f32_e32 v244, 0x42800000, v244
	v_mul_f32_e32 v245, 0x42800000, v245
	v_mul_f32_e32 v246, 0x42800000, v246
	v_mul_f32_e32 v247, 0x42800000, v247
	v_mul_f32_e32 v248, 0x42800000, v248
	v_mul_f32_e32 v249, 0x42800000, v249
	v_mul_f32_e32 v250, 0x42800000, v250
	v_mul_f32_e32 v251, 0x42800000, v251
	v_mul_f32_e32 v206, 0x42800000, v206
	v_mul_f32_e32 v207, 0x42800000, v207
	v_mul_f32_e32 v208, 0x42800000, v208
	v_mul_f32_e32 v209, 0x42800000, v209
	v_mul_f32_e32 v210, 0x42800000, v210
	v_mul_f32_e32 v211, 0x42800000, v211
	v_mul_f32_e32 v212, 0x42800000, v212
	v_mul_f32_e32 v213, 0x42800000, v213
	v_mul_f32_e32 v214, 0x42800000, v214
	v_mul_f32_e32 v215, 0x42800000, v215
	v_mul_f32_e32 v216, 0x42800000, v216
	v_mul_f32_e32 v217, 0x42800000, v217
	v_med3_f32 v232, v232, s93, v224
	v_med3_f32 v233, v233, s93, v224
	v_med3_f32 v234, v234, s93, v224
	v_med3_f32 v235, v235, s93, v224
	v_med3_f32 v236, v236, s93, v224
	v_med3_f32 v237, v237, s93, v224
	v_med3_f32 v238, v238, s93, v224
	v_med3_f32 v239, v239, s93, v224
	v_med3_f32 v240, v240, s93, v224
	v_med3_f32 v241, v241, s93, v224
	v_med3_f32 v242, v242, s93, v224
	v_med3_f32 v243, v243, s93, v224
	v_med3_f32 v244, v244, s93, v224
	v_med3_f32 v245, v245, s93, v224
	v_med3_f32 v246, v246, s93, v224
	v_med3_f32 v247, v247, s93, v224
	v_med3_f32 v248, v248, s93, v224
	v_med3_f32 v249, v249, s93, v224
	v_med3_f32 v250, v250, s93, v224
	v_med3_f32 v251, v251, s93, v224
	v_med3_f32 v206, v206, s93, v224
	v_med3_f32 v207, v207, s93, v224
	v_med3_f32 v208, v208, s93, v224
	v_med3_f32 v209, v209, s93, v224
	v_med3_f32 v210, v210, s93, v224
	v_med3_f32 v211, v211, s93, v224
	v_med3_f32 v212, v212, s93, v224
	v_med3_f32 v213, v213, s93, v224
	v_med3_f32 v214, v214, s93, v224
	v_med3_f32 v215, v215, s93, v224
	v_med3_f32 v216, v216, s93, v224
	v_med3_f32 v217, v217, s93, v224
	v_lshlrev_b32_e32 v230, 3, v226
	v_lshl_add_u32 v225, v229, s42, v230
	v_cvt_pk_fp8_f32 v252, v232, v236
	v_cvt_pk_fp8_f32 v253, v248, v206
	v_cvt_pk_fp8_f32 v252, v240, v244 op_sel:[0,0,1]
	v_cvt_pk_fp8_f32 v253, v210, v214 op_sel:[0,0,1]
	s_nop 0
	global_store_dwordx2 v225, v[252:253], s[40:41]
	v_add_u32_e32 v225, s43, v225
	v_cvt_pk_fp8_f32 v252, v233, v237
	v_cvt_pk_fp8_f32 v253, v249, v207
	v_cvt_pk_fp8_f32 v252, v241, v245 op_sel:[0,0,1]
	v_cvt_pk_fp8_f32 v253, v211, v215 op_sel:[0,0,1]
	s_nop 0
	global_store_dwordx2 v225, v[252:253], s[40:41]
	v_add_u32_e32 v225, s43, v225
	v_cvt_pk_fp8_f32 v252, v234, v238
	v_cvt_pk_fp8_f32 v253, v250, v208
	v_cvt_pk_fp8_f32 v252, v242, v246 op_sel:[0,0,1]
	v_cvt_pk_fp8_f32 v253, v212, v216 op_sel:[0,0,1]
	s_nop 0
	global_store_dwordx2 v225, v[252:253], s[40:41]
	v_add_u32_e32 v225, s43, v225
	v_cvt_pk_fp8_f32 v252, v235, v239
	v_cvt_pk_fp8_f32 v253, v251, v209
	v_cvt_pk_fp8_f32 v252, v243, v247 op_sel:[0,0,1]
	v_cvt_pk_fp8_f32 v253, v213, v217 op_sel:[0,0,1]
	s_nop 0
	global_store_dwordx2 v225, v[252:253], s[40:41]
	s_mov_b32 s42, 0
.Lilc_fd_m:
	s_and_saveexec_b64 s[0:1], s[2:3]
	s_cbranch_execz .LBB0_784
	ds_write_b32 v163, v64
	s_branch .LBB0_784
